# v23 with the fp8 loops back to full pre-barrier LDS-read waits (no fragment reads cross the phase barrier in fp8 loops; bf16 loops unchanged)
# speedup vs baseline: 1.0145x; 1.0043x over previous
.LBB0_923:
	s_add_i32 s3, s94, 0x180
	s_add_i32 s4, s36, 0x180
	s_waitcnt lgkmcnt(0)
	s_barrier
	s_setprio 1
	v_mfma_scale_f32_16x16x128_f8f6f4 v[124:127], v[24:31], v[56:63], 0, v213, v213 op_sel_hi:[0,0,0]
	v_mfma_scale_f32_16x16x128_f8f6f4 v[120:123], v[16:23], v[56:63], 0, v213, v213 op_sel_hi:[0,0,0]
	v_mfma_scale_f32_16x16x128_f8f6f4 v[116:119], v[24:31], v[48:55], 0, v213, v213 op_sel_hi:[0,0,0]
	v_mfma_scale_f32_16x16x128_f8f6f4 v[112:115], v[16:23], v[48:55], 0, v213, v213 op_sel_hi:[0,0,0]
	v_mfma_scale_f32_16x16x128_f8f6f4 v[108:111], v[24:31], v[40:47], 0, v213, v213 op_sel_hi:[0,0,0]
	v_mfma_scale_f32_16x16x128_f8f6f4 v[104:107], v[16:23], v[40:47], 0, v213, v213 op_sel_hi:[0,0,0]
	v_mfma_scale_f32_16x16x128_f8f6f4 v[100:103], v[24:31], v[32:39], 0, v213, v213 op_sel_hi:[0,0,0]
	v_mfma_scale_f32_16x16x128_f8f6f4 v[96:99], v[16:23], v[32:39], 0, v213, v213 op_sel_hi:[0,0,0]
	s_setprio 0
	s_setprio 1
	v_mfma_scale_f32_16x16x128_f8f6f4 v[92:95], v[8:15], v[56:63], 0, v213, v213 op_sel_hi:[0,0,0]
	v_mfma_scale_f32_16x16x128_f8f6f4 v[88:91], v[0:7], v[56:63], 0, v213, v213 op_sel_hi:[0,0,0]
	v_mfma_scale_f32_16x16x128_f8f6f4 v[84:87], v[8:15], v[48:55], 0, v213, v213 op_sel_hi:[0,0,0]
	v_mfma_scale_f32_16x16x128_f8f6f4 v[80:83], v[0:7], v[48:55], 0, v213, v213 op_sel_hi:[0,0,0]
	v_mfma_scale_f32_16x16x128_f8f6f4 v[76:79], v[8:15], v[40:47], 0, v213, v213 op_sel_hi:[0,0,0]
	v_mfma_scale_f32_16x16x128_f8f6f4 v[72:75], v[0:7], v[40:47], 0, v213, v213 op_sel_hi:[0,0,0]
	v_mfma_scale_f32_16x16x128_f8f6f4 v[68:71], v[8:15], v[32:39], 0, v213, v213 op_sel_hi:[0,0,0]
	v_mfma_scale_f32_16x16x128_f8f6f4 v[64:67], v[0:7], v[32:39], 0, v213, v213 op_sel_hi:[0,0,0]
	s_setprio 0
	s_barrier
	ds_read_b128 v[24:27], v217 offset:0x8000
	ds_read_b128 v[28:31], v217 offset:0x8400
	ds_read_b128 v[16:19], v217 offset:0x8800
	ds_read_b128 v[20:23], v217 offset:0x8c00
	ds_read_b128 v[32:35], v216 offset:0x8000
	ds_read_b128 v[36:39], v216 offset:0x8400
	ds_read_b128 v[40:43], v216 offset:0x8800
	ds_read_b128 v[44:47], v216 offset:0x8c00
	ds_read_b128 v[48:51], v216 offset:0x9000
	ds_read_b128 v[52:55], v216 offset:0x9400
	ds_read_b128 v[56:59], v216 offset:0x9800
	ds_read_b128 v[60:63], v216 offset:0x9c00
	ds_read_b128 v[8:11], v217 offset:0xc000
	ds_read_b128 v[12:15], v217 offset:0xc400
	ds_read_b128 v[0:3], v217 offset:0xc800
	ds_read_b128 v[4:7], v217 offset:0xcc00
	s_mov_b32 m0, s76
	s_add_i32 s5, s94, 0x80100
	buffer_load_dwordx4 v214, s[12:15], s5 offen lds
	s_add_i32 s5, s94, 0xc0100
	s_mov_b32 m0, s77
	s_nop 0
	buffer_load_dwordx4 v214, s[12:15], s5 offen lds
	s_waitcnt vmcnt(10)
	s_waitcnt lgkmcnt(0)
	s_barrier
	s_setprio 1
	v_mfma_scale_f32_16x16x128_f8f6f4 v[188:191], v[24:31], v[32:39], v[188:191], v213, v213 op_sel_hi:[0,0,0]
	v_mfma_scale_f32_16x16x128_f8f6f4 v[184:187], v[16:23], v[32:39], v[184:187], v213, v213 op_sel_hi:[0,0,0]
	v_mfma_scale_f32_16x16x128_f8f6f4 v[180:183], v[24:31], v[40:47], v[180:183], v213, v213 op_sel_hi:[0,0,0]
	v_mfma_scale_f32_16x16x128_f8f6f4 v[176:179], v[16:23], v[40:47], v[176:179], v213, v213 op_sel_hi:[0,0,0]
	v_mfma_scale_f32_16x16x128_f8f6f4 v[172:175], v[24:31], v[48:55], v[172:175], v213, v213 op_sel_hi:[0,0,0]
	v_mfma_scale_f32_16x16x128_f8f6f4 v[168:171], v[16:23], v[48:55], v[168:171], v213, v213 op_sel_hi:[0,0,0]
	v_mfma_scale_f32_16x16x128_f8f6f4 v[164:167], v[24:31], v[56:63], v[164:167], v213, v213 op_sel_hi:[0,0,0]
	v_mfma_scale_f32_16x16x128_f8f6f4 v[160:163], v[16:23], v[56:63], v[160:163], v213, v213 op_sel_hi:[0,0,0]
	s_setprio 0
	s_setprio 1
	v_mfma_scale_f32_16x16x128_f8f6f4 v[156:159], v[8:15], v[32:39], v[156:159], v213, v213 op_sel_hi:[0,0,0]
	v_mfma_scale_f32_16x16x128_f8f6f4 v[152:155], v[0:7], v[32:39], v[152:155], v213, v213 op_sel_hi:[0,0,0]
	v_mfma_scale_f32_16x16x128_f8f6f4 v[148:151], v[8:15], v[40:47], v[148:151], v213, v213 op_sel_hi:[0,0,0]
	v_mfma_scale_f32_16x16x128_f8f6f4 v[144:147], v[0:7], v[40:47], v[144:147], v213, v213 op_sel_hi:[0,0,0]
	v_mfma_scale_f32_16x16x128_f8f6f4 v[140:143], v[8:15], v[48:55], v[140:143], v213, v213 op_sel_hi:[0,0,0]
	v_mfma_scale_f32_16x16x128_f8f6f4 v[136:139], v[0:7], v[48:55], v[136:139], v213, v213 op_sel_hi:[0,0,0]
	v_mfma_scale_f32_16x16x128_f8f6f4 v[132:135], v[8:15], v[56:63], v[132:135], v213, v213 op_sel_hi:[0,0,0]
	v_mfma_scale_f32_16x16x128_f8f6f4 v[128:131], v[0:7], v[56:63], v[128:131], v213, v213 op_sel_hi:[0,0,0]
	s_setprio 0
	s_barrier
	ds_read_b128 v[32:35], v216 offset:0xc000
	ds_read_b128 v[36:39], v216 offset:0xc400
	ds_read_b128 v[40:43], v216 offset:0xc800
	ds_read_b128 v[44:47], v216 offset:0xcc00
	ds_read_b128 v[48:51], v216 offset:0xd000
	ds_read_b128 v[52:55], v216 offset:0xd400
	ds_read_b128 v[56:59], v216 offset:0xd800
	ds_read_b128 v[60:63], v216 offset:0xdc00
	s_mov_b32 m0, s80
	s_mov_b32 s10, s14
	s_mov_b32 s11, s15
	buffer_load_dwordx4 v215, s[8:11], s4 offen lds
	s_add_i32 s4, s36, 0x80180
	s_mov_b32 m0, s81
	s_nop 0
	buffer_load_dwordx4 v215, s[8:11], s4 offen lds
	s_add_i32 s4, s36, 0x8180
	s_mov_b32 m0, s84
	s_nop 0
	buffer_load_dwordx4 v215, s[8:11], s4 offen lds
	s_add_i32 s4, s36, 0x88180
	s_mov_b32 m0, s85
	s_nop 0
	buffer_load_dwordx4 v215, s[8:11], s4 offen lds
	s_mov_b32 m0, s82
	s_nop 0
	buffer_load_dwordx4 v214, s[12:15], s3 offen lds
	s_add_i32 s3, s94, 0x40180
	s_mov_b32 m0, s83
	s_nop 0
	buffer_load_dwordx4 v214, s[12:15], s3 offen lds
	s_waitcnt vmcnt(8)
	s_waitcnt lgkmcnt(0)
	s_barrier
	s_setprio 1
	v_mfma_scale_f32_16x16x128_f8f6f4 v[124:127], v[24:31], v[32:39], v[124:127], v213, v213 op_sel_hi:[0,0,0]
	v_mfma_scale_f32_16x16x128_f8f6f4 v[120:123], v[16:23], v[32:39], v[120:123], v213, v213 op_sel_hi:[0,0,0]
	v_mfma_scale_f32_16x16x128_f8f6f4 v[116:119], v[24:31], v[40:47], v[116:119], v213, v213 op_sel_hi:[0,0,0]
	v_mfma_scale_f32_16x16x128_f8f6f4 v[112:115], v[16:23], v[40:47], v[112:115], v213, v213 op_sel_hi:[0,0,0]
	v_mfma_scale_f32_16x16x128_f8f6f4 v[108:111], v[24:31], v[48:55], v[108:111], v213, v213 op_sel_hi:[0,0,0]
	v_mfma_scale_f32_16x16x128_f8f6f4 v[104:107], v[16:23], v[48:55], v[104:107], v213, v213 op_sel_hi:[0,0,0]
	v_mfma_scale_f32_16x16x128_f8f6f4 v[100:103], v[24:31], v[56:63], v[100:103], v213, v213 op_sel_hi:[0,0,0]
	v_mfma_scale_f32_16x16x128_f8f6f4 v[96:99], v[16:23], v[56:63], v[96:99], v213, v213 op_sel_hi:[0,0,0]
	s_setprio 0
	s_setprio 1
	v_mfma_scale_f32_16x16x128_f8f6f4 v[92:95], v[8:15], v[32:39], v[92:95], v213, v213 op_sel_hi:[0,0,0]
	v_mfma_scale_f32_16x16x128_f8f6f4 v[88:91], v[0:7], v[32:39], v[88:91], v213, v213 op_sel_hi:[0,0,0]
	v_mfma_scale_f32_16x16x128_f8f6f4 v[84:87], v[8:15], v[40:47], v[84:87], v213, v213 op_sel_hi:[0,0,0]
	v_mfma_scale_f32_16x16x128_f8f6f4 v[80:83], v[0:7], v[40:47], v[80:83], v213, v213 op_sel_hi:[0,0,0]
	v_mfma_scale_f32_16x16x128_f8f6f4 v[76:79], v[8:15], v[48:55], v[76:79], v213, v213 op_sel_hi:[0,0,0]
	v_mfma_scale_f32_16x16x128_f8f6f4 v[72:75], v[0:7], v[48:55], v[72:75], v213, v213 op_sel_hi:[0,0,0]
	v_mfma_scale_f32_16x16x128_f8f6f4 v[68:71], v[8:15], v[56:63], v[68:71], v213, v213 op_sel_hi:[0,0,0]
	v_mfma_scale_f32_16x16x128_f8f6f4 v[64:67], v[0:7], v[56:63], v[64:67], v213, v213 op_sel_hi:[0,0,0]
	s_setprio 0
	s_barrier
	s_waitcnt vmcnt(14)
	v_mul_f32_e32 v0, 0x42800000, v196
	v_mul_f32_e32 v1, 0x42800000, v192
	v_mul_f32_e32 v2, 0x42800000, v197
	v_mul_f32_e32 v3, 0x42800000, v193
	v_mul_f32_e32 v4, 0x42800000, v198
	v_mul_f32_e32 v5, 0x42800000, v194
	v_mul_f32_e32 v6, 0x42800000, v199
	v_mul_f32_e32 v7, 0x42800000, v195
	v_cvt_pk_fp8_f32 v202, v1, v0
	v_cvt_pk_fp8_f32 v219, v3, v2
	v_cvt_pk_fp8_f32 v220, v5, v4
	v_cvt_pk_fp8_f32 v221, v7, v6
	s_add_i32 s61, s36, 0x200
	s_mov_b32 s33, 0
	s_mov_b32 s79, s66
	s_mov_b32 s90, s68
	s_branch .LBB0_926

.LBB0_926:
	v_mov_b32_e32 v40, v202
	v_mov_b32_e32 v41, v219
	v_mov_b32_e32 v42, v220
	v_mov_b32_e32 v43, v221
	s_add_i32 s4, s94, s33
	s_mov_b32 s64, s90
	s_add_i32 s90, s90, 1
	s_add_i32 s3, s4, 0x200
	s_add_i32 s5, s61, s33
	ds_read_b128 v[24:27], v217 offset:0
	ds_read_b128 v[28:31], v217 offset:0x400
	ds_read_b128 v[16:19], v217 offset:0x800
	ds_read_b128 v[20:23], v217 offset:0xc00
	ds_read_b128 v[46:49], v216 offset:0
	ds_read_b128 v[50:53], v216 offset:0x400
	ds_read_b128 v[54:57], v216 offset:0x800
	ds_read_b128 v[58:61], v216 offset:0xc00
	ds_read_b128 v[192:195], v216 offset:0x1000
	ds_read_b128 v[196:199], v216 offset:0x1400
	ds_read_b128 v[220:223], v216 offset:0x1800
	ds_read_b128 v[224:227], v216 offset:0x1c00
	ds_read_b128 v[8:11], v217 offset:0x4000
	ds_read_b128 v[12:15], v217 offset:0x4400
	ds_read_b128 v[0:3], v217 offset:0x4800
	ds_read_b128 v[4:7], v217 offset:0x4c00
	s_cmpk_eq_i32 s33, 0xe00
	s_cselect_b32 s65, s60, s3
	s_cselect_b32 s16, s95, s5
	s_add_i32 s3, s65, 0x80
	s_mov_b32 m0, s86
	s_add_i32 s5, s4, 0x80180
	buffer_load_dwordx4 v214, s[12:15], s5 offen lds
	s_add_i32 s4, s4, 0xc0180
	s_mov_b32 m0, s89
	s_add_i32 s17, s16, 0x80
	buffer_load_dwordx4 v214, s[12:15], s4 offen lds
	s_lshr_b32 s4, s90, 2
	s_mul_i32 s5, s4, s34
	s_add_i32 s36, s5, s2
	s_cmp_lt_i32 s4, s47
	s_cselect_b64 s[4:5], -1, 0
	s_and_b64 s[62:63], s[4:5], exec
	s_cselect_b32 s67, s36, 0
	s_ashr_i32 s62, s67, 7
	s_bfe_u32 s36, s90, 0x10001
	s_ashr_i32 s63, s62, 31
	s_or_b32 s78, s36, s87
	s_bfe_u32 s36, s67, 0x20005
	s_lshl_b64 vcc, s[62:63], 23
	s_add_u32 vcc_lo, s28, vcc_lo
	s_addc_u32 vcc_hi, s29, vcc_hi
	s_lshl_b32 s38, s36, 21
	s_add_u32 s38, vcc_lo, s38
	s_addc_u32 s39, vcc_hi, 0
	s_lshl_b32 s67, s67, 7
	s_and_b32 s67, s67, 0xf80
	s_lshl_b32 vcc_lo, s67, 2
	s_add_u32 vcc_lo, s38, vcc_lo
	v_and_or_b32 v202, s79, 2, v200
	s_addc_u32 vcc_hi, s39, 0
	v_lshl_or_b32 v44, s78, 5, v218
	v_lshlrev_b64 v[32:33], 14, v[202:203]
	v_lshl_add_u64 v[32:33], vcc, 0, v[32:33]
	v_lshlrev_b32_e32 v202, 2, v44
	v_lshl_add_u64 v[32:33], v[32:33], 0, v[202:203]
	s_movk_i32 s38, 0x4000
	v_add_co_u32_e32 v36, vcc, s38, v32
	s_nop 1
	v_addc_co_u32_e32 v37, vcc, 0, v33, vcc
	global_load_dwordx4 v[32:35], v[32:33], off nt
	s_nop 0
	global_load_dwordx4 v[36:39], v[36:37], off nt
	s_waitcnt vmcnt(10)
	s_waitcnt lgkmcnt(0)
	s_barrier
	s_setprio 1
	v_mfma_scale_f32_16x16x128_f8f6f4 v[188:191], v[24:31], v[46:53], v[188:191], v213, v213 op_sel_hi:[0,0,0]
	v_mfma_scale_f32_16x16x128_f8f6f4 v[184:187], v[16:23], v[46:53], v[184:187], v213, v213 op_sel_hi:[0,0,0]
	v_mfma_scale_f32_16x16x128_f8f6f4 v[180:183], v[24:31], v[54:61], v[180:183], v213, v213 op_sel_hi:[0,0,0]
	v_mfma_scale_f32_16x16x128_f8f6f4 v[176:179], v[16:23], v[54:61], v[176:179], v213, v213 op_sel_hi:[0,0,0]
	v_mfma_scale_f32_16x16x128_f8f6f4 v[172:175], v[24:31], v[192:199], v[172:175], v213, v213 op_sel_hi:[0,0,0]
	v_mfma_scale_f32_16x16x128_f8f6f4 v[168:171], v[16:23], v[192:199], v[168:171], v213, v213 op_sel_hi:[0,0,0]
	v_mfma_scale_f32_16x16x128_f8f6f4 v[164:167], v[24:31], v[220:227], v[164:167], v213, v213 op_sel_hi:[0,0,0]
	v_mfma_scale_f32_16x16x128_f8f6f4 v[160:163], v[16:23], v[220:227], v[160:163], v213, v213 op_sel_hi:[0,0,0]
	s_setprio 0
	s_setprio 1
	v_mfma_scale_f32_16x16x128_f8f6f4 v[156:159], v[8:15], v[46:53], v[156:159], v213, v213 op_sel_hi:[0,0,0]
	v_mfma_scale_f32_16x16x128_f8f6f4 v[152:155], v[0:7], v[46:53], v[152:155], v213, v213 op_sel_hi:[0,0,0]
	v_mfma_scale_f32_16x16x128_f8f6f4 v[148:151], v[8:15], v[54:61], v[148:151], v213, v213 op_sel_hi:[0,0,0]
	v_mfma_scale_f32_16x16x128_f8f6f4 v[144:147], v[0:7], v[54:61], v[144:147], v213, v213 op_sel_hi:[0,0,0]
	v_mfma_scale_f32_16x16x128_f8f6f4 v[140:143], v[8:15], v[192:199], v[140:143], v213, v213 op_sel_hi:[0,0,0]
	v_mfma_scale_f32_16x16x128_f8f6f4 v[136:139], v[0:7], v[192:199], v[136:139], v213, v213 op_sel_hi:[0,0,0]
	v_mfma_scale_f32_16x16x128_f8f6f4 v[132:135], v[8:15], v[220:227], v[132:135], v213, v213 op_sel_hi:[0,0,0]
	v_mfma_scale_f32_16x16x128_f8f6f4 v[128:131], v[0:7], v[220:227], v[128:131], v213, v213 op_sel_hi:[0,0,0]
	s_setprio 0
	s_barrier
	ds_read_b128 v[46:49], v216 offset:0x4000
	ds_read_b128 v[50:53], v216 offset:0x4400
	ds_read_b128 v[54:57], v216 offset:0x4800
	ds_read_b128 v[58:61], v216 offset:0x4c00
	ds_read_b128 v[192:195], v216 offset:0x5000
	ds_read_b128 v[196:199], v216 offset:0x5400
	ds_read_b128 v[220:223], v216 offset:0x5800
	ds_read_b128 v[224:227], v216 offset:0x5c00
	s_mov_b32 m0, s71
	s_nop 0
	buffer_load_dwordx4 v215, s[8:11], s16 offen lds
	s_add_i32 s38, s16, 0x80000
	s_mov_b32 m0, s72
	s_nop 0
	buffer_load_dwordx4 v215, s[8:11], s38 offen lds
	s_add_i32 s38, s16, 0x8000
	s_mov_b32 m0, s73
	s_nop 0
	buffer_load_dwordx4 v215, s[8:11], s38 offen lds
	s_add_i32 s38, s16, 0x88000
	s_mov_b32 m0, s74
	s_nop 0
	buffer_load_dwordx4 v215, s[8:11], s38 offen lds
	s_mov_b32 m0, s70
	s_add_i32 s38, s65, 0x40000
	buffer_load_dwordx4 v214, s[12:15], s65 offen lds
	s_mov_b32 m0, s75
	s_nop 0
	buffer_load_dwordx4 v214, s[12:15], s38 offen lds
	s_waitcnt vmcnt(10)
	s_waitcnt lgkmcnt(0)
	s_barrier
	s_setprio 1
	v_mfma_scale_f32_16x16x128_f8f6f4 v[124:127], v[24:31], v[46:53], v[124:127], v213, v213 op_sel_hi:[0,0,0]
	v_mfma_scale_f32_16x16x128_f8f6f4 v[120:123], v[16:23], v[46:53], v[120:123], v213, v213 op_sel_hi:[0,0,0]
	v_mfma_scale_f32_16x16x128_f8f6f4 v[116:119], v[24:31], v[54:61], v[116:119], v213, v213 op_sel_hi:[0,0,0]
	v_mfma_scale_f32_16x16x128_f8f6f4 v[112:115], v[16:23], v[54:61], v[112:115], v213, v213 op_sel_hi:[0,0,0]
	v_mfma_scale_f32_16x16x128_f8f6f4 v[108:111], v[24:31], v[192:199], v[108:111], v213, v213 op_sel_hi:[0,0,0]
	v_mfma_scale_f32_16x16x128_f8f6f4 v[104:107], v[16:23], v[192:199], v[104:107], v213, v213 op_sel_hi:[0,0,0]
	v_mfma_scale_f32_16x16x128_f8f6f4 v[100:103], v[24:31], v[220:227], v[100:103], v213, v213 op_sel_hi:[0,0,0]
	v_mfma_scale_f32_16x16x128_f8f6f4 v[96:99], v[16:23], v[220:227], v[96:99], v213, v213 op_sel_hi:[0,0,0]
	s_setprio 0
	s_setprio 1
	v_mfma_scale_f32_16x16x128_f8f6f4 v[92:95], v[8:15], v[46:53], v[92:95], v213, v213 op_sel_hi:[0,0,0]
	v_mfma_scale_f32_16x16x128_f8f6f4 v[88:91], v[0:7], v[46:53], v[88:91], v213, v213 op_sel_hi:[0,0,0]
	v_mfma_scale_f32_16x16x128_f8f6f4 v[84:87], v[8:15], v[54:61], v[84:87], v213, v213 op_sel_hi:[0,0,0]
	v_mfma_scale_f32_16x16x128_f8f6f4 v[80:83], v[0:7], v[54:61], v[80:83], v213, v213 op_sel_hi:[0,0,0]
	v_mfma_scale_f32_16x16x128_f8f6f4 v[76:79], v[8:15], v[192:199], v[76:79], v213, v213 op_sel_hi:[0,0,0]
	v_mfma_scale_f32_16x16x128_f8f6f4 v[72:75], v[0:7], v[192:199], v[72:75], v213, v213 op_sel_hi:[0,0,0]
	v_mfma_scale_f32_16x16x128_f8f6f4 v[68:71], v[8:15], v[220:227], v[68:71], v213, v213 op_sel_hi:[0,0,0]
	v_mfma_scale_f32_16x16x128_f8f6f4 v[64:67], v[0:7], v[220:227], v[64:67], v213, v213 op_sel_hi:[0,0,0]
	s_setprio 0
	s_barrier
	ds_read_b128 v[16:19], v217 offset:0x8000
	ds_read_b128 v[20:23], v217 offset:0x8400
	ds_read_b128 v[24:27], v217 offset:0x8800
	ds_read_b128 v[28:31], v217 offset:0x8c00
	ds_read_b128 v[46:49], v216 offset:0x8000
	ds_read_b128 v[50:53], v216 offset:0x8400
	ds_read_b128 v[54:57], v216 offset:0x8800
	ds_read_b128 v[58:61], v216 offset:0x8c00
	ds_read_b128 v[192:195], v216 offset:0x9000
	ds_read_b128 v[196:199], v216 offset:0x9400
	ds_read_b128 v[220:223], v216 offset:0x9800
	ds_read_b128 v[224:227], v216 offset:0x9c00
	ds_read_b128 v[8:11], v217 offset:0xc000
	ds_read_b128 v[12:15], v217 offset:0xc400
	ds_read_b128 v[0:3], v217 offset:0xc800
	ds_read_b128 v[4:7], v217 offset:0xcc00
	s_mov_b32 m0, s76
	s_add_i32 s38, s65, 0x80000
	buffer_load_dwordx4 v214, s[12:15], s38 offen lds
	s_add_i32 s38, s65, 0xc0000
	s_mov_b32 m0, s77
	s_nop 0
	buffer_load_dwordx4 v214, s[12:15], s38 offen lds
	s_waitcnt vmcnt(10)
	s_waitcnt lgkmcnt(0)
	s_barrier
	s_setprio 1
	v_mfma_scale_f32_16x16x128_f8f6f4 v[188:191], v[16:23], v[46:53], v[188:191], v213, v213 op_sel_hi:[0,0,0]
	v_mfma_scale_f32_16x16x128_f8f6f4 v[184:187], v[24:31], v[46:53], v[184:187], v213, v213 op_sel_hi:[0,0,0]
	v_mfma_scale_f32_16x16x128_f8f6f4 v[180:183], v[16:23], v[54:61], v[180:183], v213, v213 op_sel_hi:[0,0,0]
	v_mfma_scale_f32_16x16x128_f8f6f4 v[176:179], v[24:31], v[54:61], v[176:179], v213, v213 op_sel_hi:[0,0,0]
	v_mfma_scale_f32_16x16x128_f8f6f4 v[172:175], v[16:23], v[192:199], v[172:175], v213, v213 op_sel_hi:[0,0,0]
	v_mfma_scale_f32_16x16x128_f8f6f4 v[168:171], v[24:31], v[192:199], v[168:171], v213, v213 op_sel_hi:[0,0,0]
	v_mfma_scale_f32_16x16x128_f8f6f4 v[164:167], v[16:23], v[220:227], v[164:167], v213, v213 op_sel_hi:[0,0,0]
	v_mfma_scale_f32_16x16x128_f8f6f4 v[160:163], v[24:31], v[220:227], v[160:163], v213, v213 op_sel_hi:[0,0,0]
	s_setprio 0
	s_setprio 1
	v_mfma_scale_f32_16x16x128_f8f6f4 v[156:159], v[8:15], v[46:53], v[156:159], v213, v213 op_sel_hi:[0,0,0]
	v_mfma_scale_f32_16x16x128_f8f6f4 v[152:155], v[0:7], v[46:53], v[152:155], v213, v213 op_sel_hi:[0,0,0]
	v_mfma_scale_f32_16x16x128_f8f6f4 v[148:151], v[8:15], v[54:61], v[148:151], v213, v213 op_sel_hi:[0,0,0]
	v_mfma_scale_f32_16x16x128_f8f6f4 v[144:147], v[0:7], v[54:61], v[144:147], v213, v213 op_sel_hi:[0,0,0]
	v_mfma_scale_f32_16x16x128_f8f6f4 v[140:143], v[8:15], v[192:199], v[140:143], v213, v213 op_sel_hi:[0,0,0]
	v_mfma_scale_f32_16x16x128_f8f6f4 v[136:139], v[0:7], v[192:199], v[136:139], v213, v213 op_sel_hi:[0,0,0]
	v_mfma_scale_f32_16x16x128_f8f6f4 v[132:135], v[8:15], v[220:227], v[132:135], v213, v213 op_sel_hi:[0,0,0]
	v_mfma_scale_f32_16x16x128_f8f6f4 v[128:131], v[0:7], v[220:227], v[128:131], v213, v213 op_sel_hi:[0,0,0]
	s_setprio 0
	s_barrier
	ds_read_b128 v[46:49], v216 offset:0xc000
	ds_read_b128 v[50:53], v216 offset:0xc400
	ds_read_b128 v[54:57], v216 offset:0xc800
	ds_read_b128 v[58:61], v216 offset:0xcc00
	ds_read_b128 v[192:195], v216 offset:0xd000
	ds_read_b128 v[196:199], v216 offset:0xd400
	ds_read_b128 v[220:223], v216 offset:0xd800
	ds_read_b128 v[224:227], v216 offset:0xdc00
	s_mov_b32 m0, s80
	s_nop 0
	buffer_load_dwordx4 v215, s[8:11], s17 offen lds
	s_add_i32 s17, s16, 0x80080
	s_mov_b32 m0, s81
	s_add_i32 s65, s65, 0x40080
	buffer_load_dwordx4 v215, s[8:11], s17 offen lds
	s_add_i32 s17, s16, 0x8080
	s_mov_b32 m0, s84
	s_add_i32 s16, s16, 0x88080
	buffer_load_dwordx4 v215, s[8:11], s17 offen lds
	s_mov_b32 m0, s85
	s_nop 0
	buffer_load_dwordx4 v215, s[8:11], s16 offen lds
	s_mov_b32 m0, s82
	s_nop 0
	buffer_load_dwordx4 v214, s[12:15], s3 offen lds
	s_mov_b32 m0, s83
	s_nop 0
	buffer_load_dwordx4 v214, s[12:15], s65 offen lds
	s_waitcnt vmcnt(8)
	s_waitcnt lgkmcnt(0)
	s_barrier
	s_setprio 1
	v_mfma_scale_f32_16x16x128_f8f6f4 v[124:127], v[16:23], v[46:53], v[124:127], v213, v213 op_sel_hi:[0,0,0]
	v_mfma_scale_f32_16x16x128_f8f6f4 v[120:123], v[24:31], v[46:53], v[120:123], v213, v213 op_sel_hi:[0,0,0]
	v_mfma_scale_f32_16x16x128_f8f6f4 v[116:119], v[16:23], v[54:61], v[116:119], v213, v213 op_sel_hi:[0,0,0]
	v_mfma_scale_f32_16x16x128_f8f6f4 v[112:115], v[24:31], v[54:61], v[112:115], v213, v213 op_sel_hi:[0,0,0]
	v_mfma_scale_f32_16x16x128_f8f6f4 v[108:111], v[16:23], v[192:199], v[108:111], v213, v213 op_sel_hi:[0,0,0]
	v_mfma_scale_f32_16x16x128_f8f6f4 v[104:107], v[24:31], v[192:199], v[104:107], v213, v213 op_sel_hi:[0,0,0]
	v_mfma_scale_f32_16x16x128_f8f6f4 v[100:103], v[16:23], v[220:227], v[100:103], v213, v213 op_sel_hi:[0,0,0]
	v_mfma_scale_f32_16x16x128_f8f6f4 v[96:99], v[24:31], v[220:227], v[96:99], v213, v213 op_sel_hi:[0,0,0]
	s_setprio 0
	s_setprio 1
	v_mfma_scale_f32_16x16x128_f8f6f4 v[92:95], v[8:15], v[46:53], v[92:95], v213, v213 op_sel_hi:[0,0,0]
	v_mfma_scale_f32_16x16x128_f8f6f4 v[88:91], v[0:7], v[46:53], v[88:91], v213, v213 op_sel_hi:[0,0,0]
	v_mfma_scale_f32_16x16x128_f8f6f4 v[84:87], v[8:15], v[54:61], v[84:87], v213, v213 op_sel_hi:[0,0,0]
	v_mfma_scale_f32_16x16x128_f8f6f4 v[80:83], v[0:7], v[54:61], v[80:83], v213, v213 op_sel_hi:[0,0,0]
	v_mfma_scale_f32_16x16x128_f8f6f4 v[76:79], v[8:15], v[192:199], v[76:79], v213, v213 op_sel_hi:[0,0,0]
	v_mfma_scale_f32_16x16x128_f8f6f4 v[72:75], v[0:7], v[192:199], v[72:75], v213, v213 op_sel_hi:[0,0,0]
	v_mfma_scale_f32_16x16x128_f8f6f4 v[68:71], v[8:15], v[220:227], v[68:71], v213, v213 op_sel_hi:[0,0,0]
	v_mfma_scale_f32_16x16x128_f8f6f4 v[64:67], v[0:7], v[220:227], v[64:67], v213, v213 op_sel_hi:[0,0,0]
	s_setprio 0
	s_barrier
	s_bitcmp0_b32 s64, 0
	s_waitcnt vmcnt(15)
	v_mul_f32_e32 v0, 0x42800000, v32
	s_waitcnt vmcnt(14)
	v_mul_f32_e32 v4, 0x42800000, v36
	v_mul_f32_e32 v1, 0x42800000, v33
	v_mul_f32_e32 v5, 0x42800000, v37
	v_mul_f32_e32 v2, 0x42800000, v34
	v_mul_f32_e32 v6, 0x42800000, v38
	v_mul_f32_e32 v3, 0x42800000, v35
	v_mul_f32_e32 v7, 0x42800000, v39
	s_mov_b64 s[64:65], -1
	s_cbranch_scc0 .LBB0_929
	s_andn2_b64 vcc, exec, s[64:65]
	s_cbranch_vccnz .LBB0_925
	s_branch .LBB0_930

.LBB0_1228:
	s_add_i32 s28, s61, 0x180
	s_add_i32 s29, s60, 0x180
	s_waitcnt lgkmcnt(0)
	s_barrier
	s_setprio 1
	v_mfma_scale_f32_16x16x128_f8f6f4 v[128:131], v[24:31], v[56:63], 0, v201, v201 op_sel_hi:[0,0,0]
	v_mfma_scale_f32_16x16x128_f8f6f4 v[124:127], v[16:23], v[56:63], 0, v201, v201 op_sel_hi:[0,0,0]
	v_mfma_scale_f32_16x16x128_f8f6f4 v[120:123], v[24:31], v[48:55], 0, v201, v201 op_sel_hi:[0,0,0]
	v_mfma_scale_f32_16x16x128_f8f6f4 v[116:119], v[16:23], v[48:55], 0, v201, v201 op_sel_hi:[0,0,0]
	v_mfma_scale_f32_16x16x128_f8f6f4 v[112:115], v[24:31], v[40:47], 0, v201, v201 op_sel_hi:[0,0,0]
	v_mfma_scale_f32_16x16x128_f8f6f4 v[108:111], v[16:23], v[40:47], 0, v201, v201 op_sel_hi:[0,0,0]
	v_mfma_scale_f32_16x16x128_f8f6f4 v[104:107], v[24:31], v[32:39], 0, v201, v201 op_sel_hi:[0,0,0]
	v_mfma_scale_f32_16x16x128_f8f6f4 v[100:103], v[16:23], v[32:39], 0, v201, v201 op_sel_hi:[0,0,0]
	s_setprio 0
	s_setprio 1
	v_mfma_scale_f32_16x16x128_f8f6f4 v[96:99], v[8:15], v[56:63], 0, v201, v201 op_sel_hi:[0,0,0]
	v_mfma_scale_f32_16x16x128_f8f6f4 v[92:95], v[0:7], v[56:63], 0, v201, v201 op_sel_hi:[0,0,0]
	v_mfma_scale_f32_16x16x128_f8f6f4 v[88:91], v[8:15], v[48:55], 0, v201, v201 op_sel_hi:[0,0,0]
	v_mfma_scale_f32_16x16x128_f8f6f4 v[84:87], v[0:7], v[48:55], 0, v201, v201 op_sel_hi:[0,0,0]
	v_mfma_scale_f32_16x16x128_f8f6f4 v[80:83], v[8:15], v[40:47], 0, v201, v201 op_sel_hi:[0,0,0]
	v_mfma_scale_f32_16x16x128_f8f6f4 v[76:79], v[0:7], v[40:47], 0, v201, v201 op_sel_hi:[0,0,0]
	v_mfma_scale_f32_16x16x128_f8f6f4 v[72:75], v[8:15], v[32:39], 0, v201, v201 op_sel_hi:[0,0,0]
	v_mfma_scale_f32_16x16x128_f8f6f4 v[68:71], v[0:7], v[32:39], 0, v201, v201 op_sel_hi:[0,0,0]
	s_setprio 0
	s_barrier
	ds_read_b128 v[24:27], v205 offset:0x8000
	ds_read_b128 v[28:31], v205 offset:0x8400
	ds_read_b128 v[16:19], v205 offset:0x8800
	ds_read_b128 v[20:23], v205 offset:0x8c00
	ds_read_b128 v[32:35], v204 offset:0x8000
	ds_read_b128 v[36:39], v204 offset:0x8400
	ds_read_b128 v[40:43], v204 offset:0x8800
	ds_read_b128 v[44:47], v204 offset:0x8c00
	ds_read_b128 v[48:51], v204 offset:0x9000
	ds_read_b128 v[52:55], v204 offset:0x9400
	ds_read_b128 v[56:59], v204 offset:0x9800
	ds_read_b128 v[60:63], v204 offset:0x9c00
	ds_read_b128 v[8:11], v205 offset:0xc000
	ds_read_b128 v[12:15], v205 offset:0xc400
	ds_read_b128 v[0:3], v205 offset:0xc800
	ds_read_b128 v[4:7], v205 offset:0xcc00
	s_mov_b32 m0, s44
	s_nop 0
	buffer_load_dwordx4 v216, s[4:7], s33 offen lds
	s_mov_b32 m0, s45
	s_nop 0
	buffer_load_dwordx4 v215, s[4:7], s33 offen lds
	s_waitcnt vmcnt(8)
	s_waitcnt lgkmcnt(0)
	s_barrier
	s_setprio 1
	v_mfma_scale_f32_16x16x128_f8f6f4 v[192:195], v[24:31], v[32:39], v[192:195], v201, v201 op_sel_hi:[0,0,0]
	v_mfma_scale_f32_16x16x128_f8f6f4 v[188:191], v[16:23], v[32:39], v[188:191], v201, v201 op_sel_hi:[0,0,0]
	v_mfma_scale_f32_16x16x128_f8f6f4 v[184:187], v[24:31], v[40:47], v[184:187], v201, v201 op_sel_hi:[0,0,0]
	v_mfma_scale_f32_16x16x128_f8f6f4 v[180:183], v[16:23], v[40:47], v[180:183], v201, v201 op_sel_hi:[0,0,0]
	v_mfma_scale_f32_16x16x128_f8f6f4 v[176:179], v[24:31], v[48:55], v[176:179], v201, v201 op_sel_hi:[0,0,0]
	v_mfma_scale_f32_16x16x128_f8f6f4 v[172:175], v[16:23], v[48:55], v[172:175], v201, v201 op_sel_hi:[0,0,0]
	v_mfma_scale_f32_16x16x128_f8f6f4 v[168:171], v[24:31], v[56:63], v[168:171], v201, v201 op_sel_hi:[0,0,0]
	v_mfma_scale_f32_16x16x128_f8f6f4 v[164:167], v[16:23], v[56:63], v[164:167], v201, v201 op_sel_hi:[0,0,0]
	s_setprio 0
	s_setprio 1
	v_mfma_scale_f32_16x16x128_f8f6f4 v[160:163], v[8:15], v[32:39], v[160:163], v201, v201 op_sel_hi:[0,0,0]
	v_mfma_scale_f32_16x16x128_f8f6f4 v[156:159], v[0:7], v[32:39], v[156:159], v201, v201 op_sel_hi:[0,0,0]
	v_mfma_scale_f32_16x16x128_f8f6f4 v[152:155], v[8:15], v[40:47], v[152:155], v201, v201 op_sel_hi:[0,0,0]
	v_mfma_scale_f32_16x16x128_f8f6f4 v[148:151], v[0:7], v[40:47], v[148:151], v201, v201 op_sel_hi:[0,0,0]
	v_mfma_scale_f32_16x16x128_f8f6f4 v[144:147], v[8:15], v[48:55], v[144:147], v201, v201 op_sel_hi:[0,0,0]
	v_mfma_scale_f32_16x16x128_f8f6f4 v[140:143], v[0:7], v[48:55], v[140:143], v201, v201 op_sel_hi:[0,0,0]
	v_mfma_scale_f32_16x16x128_f8f6f4 v[136:139], v[8:15], v[56:63], v[136:139], v201, v201 op_sel_hi:[0,0,0]
	v_mfma_scale_f32_16x16x128_f8f6f4 v[132:135], v[0:7], v[56:63], v[132:135], v201, v201 op_sel_hi:[0,0,0]
	s_setprio 0
	s_barrier
	ds_read_b128 v[32:35], v204 offset:0xc000
	ds_read_b128 v[36:39], v204 offset:0xc400
	ds_read_b128 v[40:43], v204 offset:0xc800
	ds_read_b128 v[44:47], v204 offset:0xcc00
	ds_read_b128 v[48:51], v204 offset:0xd000
	ds_read_b128 v[52:55], v204 offset:0xd400
	ds_read_b128 v[56:59], v204 offset:0xd800
	ds_read_b128 v[60:63], v204 offset:0xdc00
	s_mov_b32 m0, s48
	s_mov_b32 s10, s6
	s_mov_b32 s11, s7
	buffer_load_dwordx4 v203, s[8:11], s29 offen lds
	s_add_i32 s29, s60, 0x80180
	s_mov_b32 m0, s49
	s_nop 0
	buffer_load_dwordx4 v203, s[8:11], s29 offen lds
	s_add_i32 s29, s60, 0x8180
	s_mov_b32 m0, s62
	s_nop 0
	buffer_load_dwordx4 v203, s[8:11], s29 offen lds
	s_add_i32 s29, s60, 0x88180
	s_mov_b32 m0, s63
	s_nop 0
	buffer_load_dwordx4 v203, s[8:11], s29 offen lds
	s_mov_b32 m0, s50
	s_nop 0
	buffer_load_dwordx4 v214, s[4:7], s28 offen lds
	s_mov_b32 m0, s51
	s_nop 0
	buffer_load_dwordx4 v217, s[4:7], s28 offen lds
	s_waitcnt vmcnt(8)
	s_waitcnt lgkmcnt(0)
	s_barrier
	s_setprio 1
	v_mfma_scale_f32_16x16x128_f8f6f4 v[128:131], v[24:31], v[32:39], v[128:131], v201, v201 op_sel_hi:[0,0,0]
	v_mfma_scale_f32_16x16x128_f8f6f4 v[124:127], v[16:23], v[32:39], v[124:127], v201, v201 op_sel_hi:[0,0,0]
	v_mfma_scale_f32_16x16x128_f8f6f4 v[120:123], v[24:31], v[40:47], v[120:123], v201, v201 op_sel_hi:[0,0,0]
	v_mfma_scale_f32_16x16x128_f8f6f4 v[116:119], v[16:23], v[40:47], v[116:119], v201, v201 op_sel_hi:[0,0,0]
	v_mfma_scale_f32_16x16x128_f8f6f4 v[112:115], v[24:31], v[48:55], v[112:115], v201, v201 op_sel_hi:[0,0,0]
	v_mfma_scale_f32_16x16x128_f8f6f4 v[108:111], v[16:23], v[48:55], v[108:111], v201, v201 op_sel_hi:[0,0,0]
	v_mfma_scale_f32_16x16x128_f8f6f4 v[104:107], v[24:31], v[56:63], v[104:107], v201, v201 op_sel_hi:[0,0,0]
	v_mfma_scale_f32_16x16x128_f8f6f4 v[100:103], v[16:23], v[56:63], v[100:103], v201, v201 op_sel_hi:[0,0,0]
	s_setprio 0
	s_setprio 1
	v_mfma_scale_f32_16x16x128_f8f6f4 v[96:99], v[8:15], v[32:39], v[96:99], v201, v201 op_sel_hi:[0,0,0]
	v_mfma_scale_f32_16x16x128_f8f6f4 v[92:95], v[0:7], v[32:39], v[92:95], v201, v201 op_sel_hi:[0,0,0]
	v_mfma_scale_f32_16x16x128_f8f6f4 v[88:91], v[8:15], v[40:47], v[88:91], v201, v201 op_sel_hi:[0,0,0]
	v_mfma_scale_f32_16x16x128_f8f6f4 v[84:87], v[0:7], v[40:47], v[84:87], v201, v201 op_sel_hi:[0,0,0]
	v_mfma_scale_f32_16x16x128_f8f6f4 v[80:83], v[8:15], v[48:55], v[80:83], v201, v201 op_sel_hi:[0,0,0]
	v_mfma_scale_f32_16x16x128_f8f6f4 v[76:79], v[0:7], v[48:55], v[76:79], v201, v201 op_sel_hi:[0,0,0]
	v_mfma_scale_f32_16x16x128_f8f6f4 v[72:75], v[8:15], v[56:63], v[72:75], v201, v201 op_sel_hi:[0,0,0]
	v_mfma_scale_f32_16x16x128_f8f6f4 v[68:71], v[0:7], v[56:63], v[68:71], v201, v201 op_sel_hi:[0,0,0]
	s_setprio 0
	s_barrier
	s_waitcnt vmcnt(16)
	v_mbcnt_lo_u32_b32 v0, -1, 0
	v_mbcnt_hi_u32_b32 v0, -1, v0
	s_add_i32 s29, s60, 0x200
	v_lshl_add_u32 v0, v0, 4, s37
	v_ashrrev_i32_e32 v1, 31, v0
	v_lshrrev_b32_e32 v1, 22, v1
	v_add_u32_e32 v1, v0, v1
	v_ashrrev_i32_e32 v1, 10, v1
	v_mul_i32_i24_e32 v2, 0x400, v1
	v_sub_u32_e32 v2, v0, v2
	v_lshrrev_b32_e32 v3, 4, v2
	v_bitop3_b32 v3, v3, v2, 32 bitop3:0x6c
	v_ashrrev_i32_e32 v2, 31, v2
	v_lshrrev_b32_e32 v2, 26, v2
	v_add_u32_e32 v2, v3, v2
	v_and_b32_e32 v2, 0xc0, v2
	v_add_u32_e32 v0, 0x2000, v0
	v_sub_u32_e32 v2, v3, v2
	v_ashrrev_i32_e32 v3, 31, v0
	v_lshrrev_b32_e32 v3, 22, v3
	v_add_u32_e32 v3, v0, v3
	v_ashrrev_i32_e32 v3, 10, v3
	v_mul_i32_i24_e32 v4, 0x400, v3
	v_sub_u32_e32 v0, v0, v4
	v_lshrrev_b32_e32 v4, 4, v0
	v_bitop3_b32 v4, v4, v0, 32 bitop3:0x6c
	v_ashrrev_i32_e32 v0, 31, v0
	v_lshrrev_b32_e32 v0, 26, v0
	v_add_u32_e32 v0, v4, v0
	v_and_b32_e32 v0, 0xffc0, v0
	v_sub_u32_e32 v0, v4, v0
	v_lshrrev_b16_e32 v4, 7, v0
	v_and_b32_e32 v4, 1, v4
	v_add_u16_e32 v0, v0, v4
	v_lshlrev_b32_e32 v1, 5, v1
	v_ashrrev_i16_sdwa v2, v202, sext(v2) dst_sel:DWORD dst_unused:UNUSED_PAD src0_sel:DWORD src1_sel:BYTE_0
	v_lshlrev_b32_e32 v3, 5, v3
	v_ashrrev_i16_sdwa v0, v202, sext(v0) dst_sel:DWORD dst_unused:UNUSED_PAD src0_sel:DWORD src1_sel:BYTE_0
	v_and_b32_e32 v1, 32, v1
	v_bfe_i32 v2, v2, 0, 16
	v_and_b32_e32 v3, 32, v3
	v_bfe_i32 v0, v0, 0, 16
	v_add_lshl_u32 v1, v1, v2, 1
	v_add_lshl_u32 v0, v3, v0, 1
	v_lshl_add_u32 v32, v231, 12, v1
	v_lshl_add_u32 v33, v228, 12, v0
	v_lshl_add_u32 v34, v229, 12, v1
	v_lshl_add_u32 v35, v230, 12, v0
	s_mov_b32 s33, 0
.LBB0_1229:
	s_add_i32 s66, s28, 0x80
	s_cmp_eq_u32 s33, 28
	s_cselect_b64 vcc, -1, 0
	ds_read_b128 v[16:19], v205 offset:0
	ds_read_b128 v[20:23], v205 offset:0x400
	ds_read_b128 v[24:27], v205 offset:0x800
	ds_read_b128 v[28:31], v205 offset:0xc00
	ds_read_b128 v[36:39], v204 offset:0
	ds_read_b128 v[40:43], v204 offset:0x400
	ds_read_b128 v[44:47], v204 offset:0x800
	ds_read_b128 v[48:51], v204 offset:0xc00
	ds_read_b128 v[52:55], v204 offset:0x1000
	ds_read_b128 v[56:59], v204 offset:0x1400
	ds_read_b128 v[228:231], v204 offset:0x1800
	ds_read_b128 v[232:235], v204 offset:0x1c00
	ds_read_b128 v[8:11], v205 offset:0x4000
	ds_read_b128 v[12:15], v205 offset:0x4400
	ds_read_b128 v[0:3], v205 offset:0x4800
	ds_read_b128 v[4:7], v205 offset:0x4c00
	s_and_b64 s[60:61], vcc, exec
	s_cselect_b32 s66, s72, s66
	s_cselect_b32 s61, s73, s29
	s_add_i32 s60, s66, 0x80
	s_mov_b32 m0, s65
	s_nop 0
	buffer_load_dwordx4 v216, s[4:7], s28 offen lds
	s_mov_b32 m0, s68
	s_nop 0
	buffer_load_dwordx4 v215, s[4:7], s28 offen lds
	s_waitcnt vmcnt(8)
	s_waitcnt lgkmcnt(0)
	s_barrier
	s_setprio 1
	v_mfma_scale_f32_16x16x128_f8f6f4 v[192:195], v[16:23], v[36:43], v[192:195], v201, v201 op_sel_hi:[0,0,0]
	v_mfma_scale_f32_16x16x128_f8f6f4 v[188:191], v[24:31], v[36:43], v[188:191], v201, v201 op_sel_hi:[0,0,0]
	v_mfma_scale_f32_16x16x128_f8f6f4 v[184:187], v[16:23], v[44:51], v[184:187], v201, v201 op_sel_hi:[0,0,0]
	v_mfma_scale_f32_16x16x128_f8f6f4 v[180:183], v[24:31], v[44:51], v[180:183], v201, v201 op_sel_hi:[0,0,0]
	v_mfma_scale_f32_16x16x128_f8f6f4 v[176:179], v[16:23], v[52:59], v[176:179], v201, v201 op_sel_hi:[0,0,0]
	v_mfma_scale_f32_16x16x128_f8f6f4 v[172:175], v[24:31], v[52:59], v[172:175], v201, v201 op_sel_hi:[0,0,0]
	v_mfma_scale_f32_16x16x128_f8f6f4 v[168:171], v[16:23], v[228:235], v[168:171], v201, v201 op_sel_hi:[0,0,0]
	v_mfma_scale_f32_16x16x128_f8f6f4 v[164:167], v[24:31], v[228:235], v[164:167], v201, v201 op_sel_hi:[0,0,0]
	s_setprio 0
	s_setprio 1
	v_mfma_scale_f32_16x16x128_f8f6f4 v[160:163], v[8:15], v[36:43], v[160:163], v201, v201 op_sel_hi:[0,0,0]
	v_mfma_scale_f32_16x16x128_f8f6f4 v[156:159], v[0:7], v[36:43], v[156:159], v201, v201 op_sel_hi:[0,0,0]
	v_mfma_scale_f32_16x16x128_f8f6f4 v[152:155], v[8:15], v[44:51], v[152:155], v201, v201 op_sel_hi:[0,0,0]
	v_mfma_scale_f32_16x16x128_f8f6f4 v[148:151], v[0:7], v[44:51], v[148:151], v201, v201 op_sel_hi:[0,0,0]
	v_mfma_scale_f32_16x16x128_f8f6f4 v[144:147], v[8:15], v[52:59], v[144:147], v201, v201 op_sel_hi:[0,0,0]
	v_mfma_scale_f32_16x16x128_f8f6f4 v[140:143], v[0:7], v[52:59], v[140:143], v201, v201 op_sel_hi:[0,0,0]
	v_mfma_scale_f32_16x16x128_f8f6f4 v[136:139], v[8:15], v[228:235], v[136:139], v201, v201 op_sel_hi:[0,0,0]
	v_mfma_scale_f32_16x16x128_f8f6f4 v[132:135], v[0:7], v[228:235], v[132:135], v201, v201 op_sel_hi:[0,0,0]
	s_setprio 0
	s_barrier
	ds_read_b128 v[36:39], v204 offset:0x4000
	ds_read_b128 v[40:43], v204 offset:0x4400
	ds_read_b128 v[44:47], v204 offset:0x4800
	ds_read_b128 v[48:51], v204 offset:0x4c00
	ds_read_b128 v[52:55], v204 offset:0x5000
	ds_read_b128 v[56:59], v204 offset:0x5400
	ds_read_b128 v[228:231], v204 offset:0x5800
	ds_read_b128 v[232:235], v204 offset:0x5c00
	s_mov_b32 m0, s39
	s_nop 0
	buffer_load_dwordx4 v203, s[8:11], s61 offen lds
	s_add_i32 s67, s61, 0x80000
	s_mov_b32 m0, s40
	v_cndmask_b32_e32 v60, v214, v32, vcc
	buffer_load_dwordx4 v203, s[8:11], s67 offen lds
	s_add_i32 s67, s61, 0x8000
	s_mov_b32 m0, s41
	v_cndmask_b32_e32 v61, v217, v33, vcc
	buffer_load_dwordx4 v203, s[8:11], s67 offen lds
	s_add_i32 s67, s61, 0x88000
	s_mov_b32 m0, s42
	s_nop 0
	buffer_load_dwordx4 v203, s[8:11], s67 offen lds
	s_mov_b32 m0, s38
	s_nop 0
	buffer_load_dwordx4 v60, s[4:7], s66 offen lds
	s_mov_b32 m0, s43
	s_nop 0
	buffer_load_dwordx4 v61, s[4:7], s66 offen lds
	s_waitcnt vmcnt(8)
	s_waitcnt lgkmcnt(0)
	s_barrier
	s_setprio 1
	v_mfma_scale_f32_16x16x128_f8f6f4 v[128:131], v[16:23], v[36:43], v[128:131], v201, v201 op_sel_hi:[0,0,0]
	v_mfma_scale_f32_16x16x128_f8f6f4 v[124:127], v[24:31], v[36:43], v[124:127], v201, v201 op_sel_hi:[0,0,0]
	v_mfma_scale_f32_16x16x128_f8f6f4 v[120:123], v[16:23], v[44:51], v[120:123], v201, v201 op_sel_hi:[0,0,0]
	v_mfma_scale_f32_16x16x128_f8f6f4 v[116:119], v[24:31], v[44:51], v[116:119], v201, v201 op_sel_hi:[0,0,0]
	v_mfma_scale_f32_16x16x128_f8f6f4 v[112:115], v[16:23], v[52:59], v[112:115], v201, v201 op_sel_hi:[0,0,0]
	v_mfma_scale_f32_16x16x128_f8f6f4 v[108:111], v[24:31], v[52:59], v[108:111], v201, v201 op_sel_hi:[0,0,0]
	v_mfma_scale_f32_16x16x128_f8f6f4 v[104:107], v[16:23], v[228:235], v[104:107], v201, v201 op_sel_hi:[0,0,0]
	v_mfma_scale_f32_16x16x128_f8f6f4 v[100:103], v[24:31], v[228:235], v[100:103], v201, v201 op_sel_hi:[0,0,0]
	s_setprio 0
	s_setprio 1
	v_mfma_scale_f32_16x16x128_f8f6f4 v[96:99], v[8:15], v[36:43], v[96:99], v201, v201 op_sel_hi:[0,0,0]
	v_mfma_scale_f32_16x16x128_f8f6f4 v[92:95], v[0:7], v[36:43], v[92:95], v201, v201 op_sel_hi:[0,0,0]
	v_mfma_scale_f32_16x16x128_f8f6f4 v[88:91], v[8:15], v[44:51], v[88:91], v201, v201 op_sel_hi:[0,0,0]
	v_mfma_scale_f32_16x16x128_f8f6f4 v[84:87], v[0:7], v[44:51], v[84:87], v201, v201 op_sel_hi:[0,0,0]
	v_mfma_scale_f32_16x16x128_f8f6f4 v[80:83], v[8:15], v[52:59], v[80:83], v201, v201 op_sel_hi:[0,0,0]
	v_mfma_scale_f32_16x16x128_f8f6f4 v[76:79], v[0:7], v[52:59], v[76:79], v201, v201 op_sel_hi:[0,0,0]
	v_mfma_scale_f32_16x16x128_f8f6f4 v[72:75], v[8:15], v[228:235], v[72:75], v201, v201 op_sel_hi:[0,0,0]
	v_mfma_scale_f32_16x16x128_f8f6f4 v[68:71], v[0:7], v[228:235], v[68:71], v201, v201 op_sel_hi:[0,0,0]
	s_setprio 0
	s_barrier
	ds_read_b128 v[24:27], v205 offset:0x8000
	ds_read_b128 v[28:31], v205 offset:0x8400
	ds_read_b128 v[16:19], v205 offset:0x8800
	ds_read_b128 v[20:23], v205 offset:0x8c00
	ds_read_b128 v[36:39], v204 offset:0x8000
	ds_read_b128 v[40:43], v204 offset:0x8400
	ds_read_b128 v[44:47], v204 offset:0x8800
	ds_read_b128 v[48:51], v204 offset:0x8c00
	ds_read_b128 v[52:55], v204 offset:0x9000
	ds_read_b128 v[56:59], v204 offset:0x9400
	ds_read_b128 v[228:231], v204 offset:0x9800
	ds_read_b128 v[232:235], v204 offset:0x9c00
	ds_read_b128 v[8:11], v205 offset:0xc000
	ds_read_b128 v[12:15], v205 offset:0xc400
	ds_read_b128 v[0:3], v205 offset:0xc800
	ds_read_b128 v[4:7], v205 offset:0xcc00
	s_mov_b32 m0, s44
	v_cndmask_b32_e32 v62, v216, v34, vcc
	buffer_load_dwordx4 v62, s[4:7], s66 offen lds
	v_cndmask_b32_e32 v62, v215, v35, vcc
	s_mov_b32 m0, s45
	s_nop 0
	buffer_load_dwordx4 v62, s[4:7], s66 offen lds
	s_waitcnt vmcnt(8)
	s_waitcnt lgkmcnt(0)
	s_barrier
	s_setprio 1
	v_mfma_scale_f32_16x16x128_f8f6f4 v[192:195], v[24:31], v[36:43], v[192:195], v201, v201 op_sel_hi:[0,0,0]
	v_mfma_scale_f32_16x16x128_f8f6f4 v[188:191], v[16:23], v[36:43], v[188:191], v201, v201 op_sel_hi:[0,0,0]
	v_mfma_scale_f32_16x16x128_f8f6f4 v[184:187], v[24:31], v[44:51], v[184:187], v201, v201 op_sel_hi:[0,0,0]
	v_mfma_scale_f32_16x16x128_f8f6f4 v[180:183], v[16:23], v[44:51], v[180:183], v201, v201 op_sel_hi:[0,0,0]
	v_mfma_scale_f32_16x16x128_f8f6f4 v[176:179], v[24:31], v[52:59], v[176:179], v201, v201 op_sel_hi:[0,0,0]
	v_mfma_scale_f32_16x16x128_f8f6f4 v[172:175], v[16:23], v[52:59], v[172:175], v201, v201 op_sel_hi:[0,0,0]
	v_mfma_scale_f32_16x16x128_f8f6f4 v[168:171], v[24:31], v[228:235], v[168:171], v201, v201 op_sel_hi:[0,0,0]
	v_mfma_scale_f32_16x16x128_f8f6f4 v[164:167], v[16:23], v[228:235], v[164:167], v201, v201 op_sel_hi:[0,0,0]
	s_setprio 0
	s_setprio 1
	v_mfma_scale_f32_16x16x128_f8f6f4 v[160:163], v[8:15], v[36:43], v[160:163], v201, v201 op_sel_hi:[0,0,0]
	v_mfma_scale_f32_16x16x128_f8f6f4 v[156:159], v[0:7], v[36:43], v[156:159], v201, v201 op_sel_hi:[0,0,0]
	v_mfma_scale_f32_16x16x128_f8f6f4 v[152:155], v[8:15], v[44:51], v[152:155], v201, v201 op_sel_hi:[0,0,0]
	v_mfma_scale_f32_16x16x128_f8f6f4 v[148:151], v[0:7], v[44:51], v[148:151], v201, v201 op_sel_hi:[0,0,0]
	v_mfma_scale_f32_16x16x128_f8f6f4 v[144:147], v[8:15], v[52:59], v[144:147], v201, v201 op_sel_hi:[0,0,0]
	v_mfma_scale_f32_16x16x128_f8f6f4 v[140:143], v[0:7], v[52:59], v[140:143], v201, v201 op_sel_hi:[0,0,0]
	v_mfma_scale_f32_16x16x128_f8f6f4 v[136:139], v[8:15], v[228:235], v[136:139], v201, v201 op_sel_hi:[0,0,0]
	v_mfma_scale_f32_16x16x128_f8f6f4 v[132:135], v[0:7], v[228:235], v[132:135], v201, v201 op_sel_hi:[0,0,0]
	s_setprio 0
	s_barrier
	ds_read_b128 v[36:39], v204 offset:0xc000
	ds_read_b128 v[40:43], v204 offset:0xc400
	ds_read_b128 v[44:47], v204 offset:0xc800
	ds_read_b128 v[48:51], v204 offset:0xcc00
	ds_read_b128 v[52:55], v204 offset:0xd000
	ds_read_b128 v[56:59], v204 offset:0xd400
	ds_read_b128 v[228:231], v204 offset:0xd800
	ds_read_b128 v[232:235], v204 offset:0xdc00
	s_mov_b32 m0, s48
	s_add_i32 s66, s61, 0x80
	buffer_load_dwordx4 v203, s[8:11], s66 offen lds
	s_add_i32 s66, s61, 0x80080
	s_mov_b32 m0, s49
	s_nop 0
	buffer_load_dwordx4 v203, s[8:11], s66 offen lds
	s_add_i32 s66, s61, 0x8080
	s_mov_b32 m0, s62
	s_add_i32 s61, s61, 0x88080
	buffer_load_dwordx4 v203, s[8:11], s66 offen lds
	s_mov_b32 m0, s63
	s_nop 0
	buffer_load_dwordx4 v203, s[8:11], s61 offen lds
	s_mov_b32 m0, s50
	s_nop 0
	buffer_load_dwordx4 v60, s[4:7], s60 offen lds
	s_mov_b32 m0, s51
	s_nop 0
	buffer_load_dwordx4 v61, s[4:7], s60 offen lds
	s_waitcnt vmcnt(8)
	s_waitcnt lgkmcnt(0)
	s_barrier
	s_setprio 1
	v_mfma_scale_f32_16x16x128_f8f6f4 v[128:131], v[24:31], v[36:43], v[128:131], v201, v201 op_sel_hi:[0,0,0]
	v_mfma_scale_f32_16x16x128_f8f6f4 v[124:127], v[16:23], v[36:43], v[124:127], v201, v201 op_sel_hi:[0,0,0]
	v_mfma_scale_f32_16x16x128_f8f6f4 v[120:123], v[24:31], v[44:51], v[120:123], v201, v201 op_sel_hi:[0,0,0]
	v_mfma_scale_f32_16x16x128_f8f6f4 v[116:119], v[16:23], v[44:51], v[116:119], v201, v201 op_sel_hi:[0,0,0]
	v_mfma_scale_f32_16x16x128_f8f6f4 v[112:115], v[24:31], v[52:59], v[112:115], v201, v201 op_sel_hi:[0,0,0]
	v_mfma_scale_f32_16x16x128_f8f6f4 v[108:111], v[16:23], v[52:59], v[108:111], v201, v201 op_sel_hi:[0,0,0]
	v_mfma_scale_f32_16x16x128_f8f6f4 v[104:107], v[24:31], v[228:235], v[104:107], v201, v201 op_sel_hi:[0,0,0]
	v_mfma_scale_f32_16x16x128_f8f6f4 v[100:103], v[16:23], v[228:235], v[100:103], v201, v201 op_sel_hi:[0,0,0]
	s_setprio 0
	s_setprio 1
	v_mfma_scale_f32_16x16x128_f8f6f4 v[96:99], v[8:15], v[36:43], v[96:99], v201, v201 op_sel_hi:[0,0,0]
	v_mfma_scale_f32_16x16x128_f8f6f4 v[92:95], v[0:7], v[36:43], v[92:95], v201, v201 op_sel_hi:[0,0,0]
	v_mfma_scale_f32_16x16x128_f8f6f4 v[88:91], v[8:15], v[44:51], v[88:91], v201, v201 op_sel_hi:[0,0,0]
	v_mfma_scale_f32_16x16x128_f8f6f4 v[84:87], v[0:7], v[44:51], v[84:87], v201, v201 op_sel_hi:[0,0,0]
	v_mfma_scale_f32_16x16x128_f8f6f4 v[80:83], v[8:15], v[52:59], v[80:83], v201, v201 op_sel_hi:[0,0,0]
	v_mfma_scale_f32_16x16x128_f8f6f4 v[76:79], v[0:7], v[52:59], v[76:79], v201, v201 op_sel_hi:[0,0,0]
	v_mfma_scale_f32_16x16x128_f8f6f4 v[72:75], v[8:15], v[228:235], v[72:75], v201, v201 op_sel_hi:[0,0,0]
	v_mfma_scale_f32_16x16x128_f8f6f4 v[68:71], v[0:7], v[228:235], v[68:71], v201, v201 op_sel_hi:[0,0,0]
	s_setprio 0
	s_barrier
	s_add_i32 s33, s33, 2
	s_addk_i32 s28, 0x100
	s_addk_i32 s29, 0x100
	s_cmp_gt_u32 s33, 29
	s_cbranch_scc0 .LBB0_1229
	s_and_b64 vcc, exec, s[18:19]
	s_cbranch_vccz .LBB0_1232
	s_barrier

.LBB0_1329:
	s_add_i32 s36, s89, 0x180
	s_add_i32 s37, s61, 0x180
	s_waitcnt lgkmcnt(0)
	s_barrier
	s_setprio 1
	v_mfma_scale_f32_16x16x128_f8f6f4 v[128:131], v[24:31], v[56:63], 0, v198, v198 op_sel_hi:[0,0,0]
	v_mfma_scale_f32_16x16x128_f8f6f4 v[124:127], v[16:23], v[56:63], 0, v198, v198 op_sel_hi:[0,0,0]
	v_mfma_scale_f32_16x16x128_f8f6f4 v[120:123], v[24:31], v[48:55], 0, v198, v198 op_sel_hi:[0,0,0]
	v_mfma_scale_f32_16x16x128_f8f6f4 v[116:119], v[16:23], v[48:55], 0, v198, v198 op_sel_hi:[0,0,0]
	v_mfma_scale_f32_16x16x128_f8f6f4 v[112:115], v[24:31], v[40:47], 0, v198, v198 op_sel_hi:[0,0,0]
	v_mfma_scale_f32_16x16x128_f8f6f4 v[108:111], v[16:23], v[40:47], 0, v198, v198 op_sel_hi:[0,0,0]
	v_mfma_scale_f32_16x16x128_f8f6f4 v[104:107], v[24:31], v[32:39], 0, v198, v198 op_sel_hi:[0,0,0]
	v_mfma_scale_f32_16x16x128_f8f6f4 v[100:103], v[16:23], v[32:39], 0, v198, v198 op_sel_hi:[0,0,0]
	s_setprio 0
	s_setprio 1
	v_mfma_scale_f32_16x16x128_f8f6f4 v[96:99], v[8:15], v[56:63], 0, v198, v198 op_sel_hi:[0,0,0]
	v_mfma_scale_f32_16x16x128_f8f6f4 v[92:95], v[0:7], v[56:63], 0, v198, v198 op_sel_hi:[0,0,0]
	v_mfma_scale_f32_16x16x128_f8f6f4 v[88:91], v[8:15], v[48:55], 0, v198, v198 op_sel_hi:[0,0,0]
	v_mfma_scale_f32_16x16x128_f8f6f4 v[84:87], v[0:7], v[48:55], 0, v198, v198 op_sel_hi:[0,0,0]
	v_mfma_scale_f32_16x16x128_f8f6f4 v[80:83], v[8:15], v[40:47], 0, v198, v198 op_sel_hi:[0,0,0]
	v_mfma_scale_f32_16x16x128_f8f6f4 v[76:79], v[0:7], v[40:47], 0, v198, v198 op_sel_hi:[0,0,0]
	v_mfma_scale_f32_16x16x128_f8f6f4 v[72:75], v[8:15], v[32:39], 0, v198, v198 op_sel_hi:[0,0,0]
	v_mfma_scale_f32_16x16x128_f8f6f4 v[68:71], v[0:7], v[32:39], 0, v198, v198 op_sel_hi:[0,0,0]
	s_setprio 0
	s_barrier
	ds_read_b128 v[24:27], v202 offset:0x8000
	ds_read_b128 v[28:31], v202 offset:0x8400
	ds_read_b128 v[16:19], v202 offset:0x8800
	ds_read_b128 v[20:23], v202 offset:0x8c00
	ds_read_b128 v[32:35], v201 offset:0x8000
	ds_read_b128 v[36:39], v201 offset:0x8400
	ds_read_b128 v[40:43], v201 offset:0x8800
	ds_read_b128 v[44:47], v201 offset:0x8c00
	ds_read_b128 v[48:51], v201 offset:0x9000
	ds_read_b128 v[52:55], v201 offset:0x9400
	ds_read_b128 v[56:59], v201 offset:0x9800
	ds_read_b128 v[60:63], v201 offset:0x9c00
	ds_read_b128 v[8:11], v202 offset:0xc000
	ds_read_b128 v[12:15], v202 offset:0xc400
	ds_read_b128 v[0:3], v202 offset:0xc800
	ds_read_b128 v[4:7], v202 offset:0xcc00
	s_mov_b32 m0, s50
	s_nop 0
	buffer_load_dwordx4 v207, s[4:7], s33 offen lds
	s_mov_b32 m0, s51
	s_nop 0
	buffer_load_dwordx4 v206, s[4:7], s33 offen lds
	s_waitcnt vmcnt(8)
	s_waitcnt lgkmcnt(0)
	s_barrier
	s_setprio 1
	v_mfma_scale_f32_16x16x128_f8f6f4 v[192:195], v[24:31], v[32:39], v[192:195], v198, v198 op_sel_hi:[0,0,0]
	v_mfma_scale_f32_16x16x128_f8f6f4 v[188:191], v[16:23], v[32:39], v[188:191], v198, v198 op_sel_hi:[0,0,0]
	v_mfma_scale_f32_16x16x128_f8f6f4 v[184:187], v[24:31], v[40:47], v[184:187], v198, v198 op_sel_hi:[0,0,0]
	v_mfma_scale_f32_16x16x128_f8f6f4 v[180:183], v[16:23], v[40:47], v[180:183], v198, v198 op_sel_hi:[0,0,0]
	v_mfma_scale_f32_16x16x128_f8f6f4 v[176:179], v[24:31], v[48:55], v[176:179], v198, v198 op_sel_hi:[0,0,0]
	v_mfma_scale_f32_16x16x128_f8f6f4 v[172:175], v[16:23], v[48:55], v[172:175], v198, v198 op_sel_hi:[0,0,0]
	v_mfma_scale_f32_16x16x128_f8f6f4 v[168:171], v[24:31], v[56:63], v[168:171], v198, v198 op_sel_hi:[0,0,0]
	v_mfma_scale_f32_16x16x128_f8f6f4 v[164:167], v[16:23], v[56:63], v[164:167], v198, v198 op_sel_hi:[0,0,0]
	s_setprio 0
	s_setprio 1
	v_mfma_scale_f32_16x16x128_f8f6f4 v[160:163], v[8:15], v[32:39], v[160:163], v198, v198 op_sel_hi:[0,0,0]
	v_mfma_scale_f32_16x16x128_f8f6f4 v[156:159], v[0:7], v[32:39], v[156:159], v198, v198 op_sel_hi:[0,0,0]
	v_mfma_scale_f32_16x16x128_f8f6f4 v[152:155], v[8:15], v[40:47], v[152:155], v198, v198 op_sel_hi:[0,0,0]
	v_mfma_scale_f32_16x16x128_f8f6f4 v[148:151], v[0:7], v[40:47], v[148:151], v198, v198 op_sel_hi:[0,0,0]
	v_mfma_scale_f32_16x16x128_f8f6f4 v[144:147], v[8:15], v[48:55], v[144:147], v198, v198 op_sel_hi:[0,0,0]
	v_mfma_scale_f32_16x16x128_f8f6f4 v[140:143], v[0:7], v[48:55], v[140:143], v198, v198 op_sel_hi:[0,0,0]
	v_mfma_scale_f32_16x16x128_f8f6f4 v[136:139], v[8:15], v[56:63], v[136:139], v198, v198 op_sel_hi:[0,0,0]
	v_mfma_scale_f32_16x16x128_f8f6f4 v[132:135], v[0:7], v[56:63], v[132:135], v198, v198 op_sel_hi:[0,0,0]
	s_setprio 0
	s_barrier
	ds_read_b128 v[32:35], v201 offset:0xc000
	ds_read_b128 v[36:39], v201 offset:0xc400
	ds_read_b128 v[40:43], v201 offset:0xc800
	ds_read_b128 v[44:47], v201 offset:0xcc00
	ds_read_b128 v[48:51], v201 offset:0xd000
	ds_read_b128 v[52:55], v201 offset:0xd400
	ds_read_b128 v[56:59], v201 offset:0xd800
	ds_read_b128 v[60:63], v201 offset:0xdc00
	s_mov_b32 m0, s64
	s_mov_b32 s10, s6
	s_mov_b32 s11, s7
	buffer_load_dwordx4 v200, s[8:11], s37 offen lds
	s_add_i32 s33, s61, 0x80180
	s_mov_b32 m0, s65
	s_nop 0
	buffer_load_dwordx4 v200, s[8:11], s33 offen lds
	s_add_i32 s33, s61, 0x8180
	s_mov_b32 m0, s70
	s_nop 0
	buffer_load_dwordx4 v200, s[8:11], s33 offen lds
	s_add_i32 s33, s61, 0x88180
	s_mov_b32 m0, s71
	s_nop 0
	buffer_load_dwordx4 v200, s[8:11], s33 offen lds
	s_mov_b32 m0, s68
	s_nop 0
	buffer_load_dwordx4 v205, s[4:7], s36 offen lds
	s_mov_b32 m0, s69
	s_nop 0
	buffer_load_dwordx4 v208, s[4:7], s36 offen lds
	s_waitcnt vmcnt(8)
	s_waitcnt lgkmcnt(0)
	s_barrier
	s_setprio 1
	v_mfma_scale_f32_16x16x128_f8f6f4 v[128:131], v[24:31], v[32:39], v[128:131], v198, v198 op_sel_hi:[0,0,0]
	v_mfma_scale_f32_16x16x128_f8f6f4 v[124:127], v[16:23], v[32:39], v[124:127], v198, v198 op_sel_hi:[0,0,0]
	v_mfma_scale_f32_16x16x128_f8f6f4 v[120:123], v[24:31], v[40:47], v[120:123], v198, v198 op_sel_hi:[0,0,0]
	v_mfma_scale_f32_16x16x128_f8f6f4 v[116:119], v[16:23], v[40:47], v[116:119], v198, v198 op_sel_hi:[0,0,0]
	v_mfma_scale_f32_16x16x128_f8f6f4 v[112:115], v[24:31], v[48:55], v[112:115], v198, v198 op_sel_hi:[0,0,0]
	v_mfma_scale_f32_16x16x128_f8f6f4 v[108:111], v[16:23], v[48:55], v[108:111], v198, v198 op_sel_hi:[0,0,0]
	v_mfma_scale_f32_16x16x128_f8f6f4 v[104:107], v[24:31], v[56:63], v[104:107], v198, v198 op_sel_hi:[0,0,0]
	v_mfma_scale_f32_16x16x128_f8f6f4 v[100:103], v[16:23], v[56:63], v[100:103], v198, v198 op_sel_hi:[0,0,0]
	s_setprio 0
	s_setprio 1
	v_mfma_scale_f32_16x16x128_f8f6f4 v[96:99], v[8:15], v[32:39], v[96:99], v198, v198 op_sel_hi:[0,0,0]
	v_mfma_scale_f32_16x16x128_f8f6f4 v[92:95], v[0:7], v[32:39], v[92:95], v198, v198 op_sel_hi:[0,0,0]
	v_mfma_scale_f32_16x16x128_f8f6f4 v[88:91], v[8:15], v[40:47], v[88:91], v198, v198 op_sel_hi:[0,0,0]
	v_mfma_scale_f32_16x16x128_f8f6f4 v[84:87], v[0:7], v[40:47], v[84:87], v198, v198 op_sel_hi:[0,0,0]
	v_mfma_scale_f32_16x16x128_f8f6f4 v[80:83], v[8:15], v[48:55], v[80:83], v198, v198 op_sel_hi:[0,0,0]
	v_mfma_scale_f32_16x16x128_f8f6f4 v[76:79], v[0:7], v[48:55], v[76:79], v198, v198 op_sel_hi:[0,0,0]
	v_mfma_scale_f32_16x16x128_f8f6f4 v[72:75], v[8:15], v[56:63], v[72:75], v198, v198 op_sel_hi:[0,0,0]
	v_mfma_scale_f32_16x16x128_f8f6f4 v[68:71], v[0:7], v[56:63], v[68:71], v198, v198 op_sel_hi:[0,0,0]
	s_setprio 0
	s_barrier
	s_waitcnt vmcnt(16)
	v_mbcnt_lo_u32_b32 v0, -1, 0
	v_mbcnt_hi_u32_b32 v0, -1, v0
	s_add_i32 s33, s61, 0x200
	v_lshl_add_u32 v0, v0, 4, s40
	v_ashrrev_i32_e32 v1, 31, v0
	v_lshrrev_b32_e32 v1, 22, v1
	v_add_u32_e32 v1, v0, v1
	v_ashrrev_i32_e32 v1, 10, v1
	v_mul_i32_i24_e32 v2, 0x400, v1
	v_sub_u32_e32 v2, v0, v2
	v_lshrrev_b32_e32 v3, 4, v2
	v_bitop3_b32 v3, v3, v2, 32 bitop3:0x6c
	v_ashrrev_i32_e32 v2, 31, v2
	v_lshrrev_b32_e32 v2, 26, v2
	v_add_u32_e32 v2, v3, v2
	v_and_b32_e32 v2, 0xc0, v2
	v_add_u32_e32 v0, 0x2000, v0
	v_sub_u32_e32 v2, v3, v2
	v_ashrrev_i32_e32 v3, 31, v0
	v_lshrrev_b32_e32 v3, 22, v3
	v_add_u32_e32 v3, v0, v3
	v_ashrrev_i32_e32 v3, 10, v3
	v_mul_i32_i24_e32 v4, 0x400, v3
	v_sub_u32_e32 v0, v0, v4
	v_lshrrev_b32_e32 v4, 4, v0
	v_bitop3_b32 v4, v4, v0, 32 bitop3:0x6c
	v_ashrrev_i32_e32 v0, 31, v0
	v_lshrrev_b32_e32 v0, 26, v0
	v_add_u32_e32 v0, v4, v0
	v_and_b32_e32 v0, 0xffc0, v0
	v_sub_u32_e32 v0, v4, v0
	v_lshrrev_b16_e32 v4, 7, v0
	v_and_b32_e32 v4, 1, v4
	v_add_u16_e32 v0, v0, v4
	v_lshlrev_b32_e32 v1, 5, v1
	v_ashrrev_i16_sdwa v2, v199, sext(v2) dst_sel:DWORD dst_unused:UNUSED_PAD src0_sel:DWORD src1_sel:BYTE_0
	v_lshlrev_b32_e32 v3, 5, v3
	v_ashrrev_i16_sdwa v0, v199, sext(v0) dst_sel:DWORD dst_unused:UNUSED_PAD src0_sel:DWORD src1_sel:BYTE_0
	v_and_b32_e32 v1, 32, v1
	v_bfe_i32 v2, v2, 0, 16
	v_and_b32_e32 v3, 32, v3
	v_bfe_i32 v0, v0, 0, 16
	v_add_lshl_u32 v1, v1, v2, 1
	v_add_lshl_u32 v0, v3, v0, 1
	v_lshl_add_u32 v32, v220, 12, v1
	v_lshl_add_u32 v33, v217, 12, v0
	v_lshl_add_u32 v34, v218, 12, v1
	v_lshl_add_u32 v35, v219, 12, v0
	s_mov_b32 s37, 0
.LBB0_1330:
	s_add_i32 s61, s36, 0x80
	s_cmp_eq_u32 s37, 28
	s_cselect_b64 vcc, -1, 0
	ds_read_b128 v[16:19], v202 offset:0
	ds_read_b128 v[20:23], v202 offset:0x400
	ds_read_b128 v[24:27], v202 offset:0x800
	ds_read_b128 v[28:31], v202 offset:0xc00
	ds_read_b128 v[36:39], v201 offset:0
	ds_read_b128 v[40:43], v201 offset:0x400
	ds_read_b128 v[44:47], v201 offset:0x800
	ds_read_b128 v[48:51], v201 offset:0xc00
	ds_read_b128 v[52:55], v201 offset:0x1000
	ds_read_b128 v[56:59], v201 offset:0x1400
	ds_read_b128 v[218:221], v201 offset:0x1800
	ds_read_b128 v[222:225], v201 offset:0x1c00
	ds_read_b128 v[8:11], v202 offset:0x4000
	ds_read_b128 v[12:15], v202 offset:0x4400
	ds_read_b128 v[0:3], v202 offset:0x4800
	ds_read_b128 v[4:7], v202 offset:0x4c00
	s_and_b64 s[66:67], vcc, exec
	s_cselect_b32 s67, s85, s61
	s_cselect_b32 s66, s86, s33
	s_add_i32 s61, s67, 0x80
	s_mov_b32 m0, s73
	s_nop 0
	buffer_load_dwordx4 v207, s[4:7], s36 offen lds
	s_mov_b32 m0, s74
	s_nop 0
	buffer_load_dwordx4 v206, s[4:7], s36 offen lds
	s_waitcnt vmcnt(8)
	s_waitcnt lgkmcnt(0)
	s_barrier
	s_setprio 1
	v_mfma_scale_f32_16x16x128_f8f6f4 v[192:195], v[16:23], v[36:43], v[192:195], v198, v198 op_sel_hi:[0,0,0]
	v_mfma_scale_f32_16x16x128_f8f6f4 v[188:191], v[24:31], v[36:43], v[188:191], v198, v198 op_sel_hi:[0,0,0]
	v_mfma_scale_f32_16x16x128_f8f6f4 v[184:187], v[16:23], v[44:51], v[184:187], v198, v198 op_sel_hi:[0,0,0]
	v_mfma_scale_f32_16x16x128_f8f6f4 v[180:183], v[24:31], v[44:51], v[180:183], v198, v198 op_sel_hi:[0,0,0]
	v_mfma_scale_f32_16x16x128_f8f6f4 v[176:179], v[16:23], v[52:59], v[176:179], v198, v198 op_sel_hi:[0,0,0]
	v_mfma_scale_f32_16x16x128_f8f6f4 v[172:175], v[24:31], v[52:59], v[172:175], v198, v198 op_sel_hi:[0,0,0]
	v_mfma_scale_f32_16x16x128_f8f6f4 v[168:171], v[16:23], v[218:225], v[168:171], v198, v198 op_sel_hi:[0,0,0]
	v_mfma_scale_f32_16x16x128_f8f6f4 v[164:167], v[24:31], v[218:225], v[164:167], v198, v198 op_sel_hi:[0,0,0]
	s_setprio 0
	s_setprio 1
	v_mfma_scale_f32_16x16x128_f8f6f4 v[160:163], v[8:15], v[36:43], v[160:163], v198, v198 op_sel_hi:[0,0,0]
	v_mfma_scale_f32_16x16x128_f8f6f4 v[156:159], v[0:7], v[36:43], v[156:159], v198, v198 op_sel_hi:[0,0,0]
	v_mfma_scale_f32_16x16x128_f8f6f4 v[152:155], v[8:15], v[44:51], v[152:155], v198, v198 op_sel_hi:[0,0,0]
	v_mfma_scale_f32_16x16x128_f8f6f4 v[148:151], v[0:7], v[44:51], v[148:151], v198, v198 op_sel_hi:[0,0,0]
	v_mfma_scale_f32_16x16x128_f8f6f4 v[144:147], v[8:15], v[52:59], v[144:147], v198, v198 op_sel_hi:[0,0,0]
	v_mfma_scale_f32_16x16x128_f8f6f4 v[140:143], v[0:7], v[52:59], v[140:143], v198, v198 op_sel_hi:[0,0,0]
	v_mfma_scale_f32_16x16x128_f8f6f4 v[136:139], v[8:15], v[218:225], v[136:139], v198, v198 op_sel_hi:[0,0,0]
	v_mfma_scale_f32_16x16x128_f8f6f4 v[132:135], v[0:7], v[218:225], v[132:135], v198, v198 op_sel_hi:[0,0,0]
	s_setprio 0
	s_barrier
	ds_read_b128 v[36:39], v201 offset:0x4000
	ds_read_b128 v[40:43], v201 offset:0x4400
	ds_read_b128 v[44:47], v201 offset:0x4800
	ds_read_b128 v[48:51], v201 offset:0x4c00
	ds_read_b128 v[52:55], v201 offset:0x5000
	ds_read_b128 v[56:59], v201 offset:0x5400
	ds_read_b128 v[218:221], v201 offset:0x5800
	ds_read_b128 v[222:225], v201 offset:0x5c00
	s_mov_b32 m0, s45
	s_nop 0
	buffer_load_dwordx4 v200, s[8:11], s66 offen lds
	s_add_i32 s89, s66, 0x80000
	s_mov_b32 m0, s46
	v_cndmask_b32_e32 v60, v205, v32, vcc
	buffer_load_dwordx4 v200, s[8:11], s89 offen lds
	s_add_i32 s89, s66, 0x8000
	s_mov_b32 m0, s47
	v_cndmask_b32_e32 v61, v208, v33, vcc
	buffer_load_dwordx4 v200, s[8:11], s89 offen lds
	s_add_i32 s89, s66, 0x88000
	s_mov_b32 m0, s48
	s_nop 0
	buffer_load_dwordx4 v200, s[8:11], s89 offen lds
	s_mov_b32 m0, s44
	s_nop 0
	buffer_load_dwordx4 v60, s[4:7], s67 offen lds
	s_mov_b32 m0, s49
	s_nop 0
	buffer_load_dwordx4 v61, s[4:7], s67 offen lds
	s_waitcnt vmcnt(8)
	s_waitcnt lgkmcnt(0)
	s_barrier
	s_setprio 1
	v_mfma_scale_f32_16x16x128_f8f6f4 v[128:131], v[16:23], v[36:43], v[128:131], v198, v198 op_sel_hi:[0,0,0]
	v_mfma_scale_f32_16x16x128_f8f6f4 v[124:127], v[24:31], v[36:43], v[124:127], v198, v198 op_sel_hi:[0,0,0]
	v_mfma_scale_f32_16x16x128_f8f6f4 v[120:123], v[16:23], v[44:51], v[120:123], v198, v198 op_sel_hi:[0,0,0]
	v_mfma_scale_f32_16x16x128_f8f6f4 v[116:119], v[24:31], v[44:51], v[116:119], v198, v198 op_sel_hi:[0,0,0]
	v_mfma_scale_f32_16x16x128_f8f6f4 v[112:115], v[16:23], v[52:59], v[112:115], v198, v198 op_sel_hi:[0,0,0]
	v_mfma_scale_f32_16x16x128_f8f6f4 v[108:111], v[24:31], v[52:59], v[108:111], v198, v198 op_sel_hi:[0,0,0]
	v_mfma_scale_f32_16x16x128_f8f6f4 v[104:107], v[16:23], v[218:225], v[104:107], v198, v198 op_sel_hi:[0,0,0]
	v_mfma_scale_f32_16x16x128_f8f6f4 v[100:103], v[24:31], v[218:225], v[100:103], v198, v198 op_sel_hi:[0,0,0]
	s_setprio 0
	s_setprio 1
	v_mfma_scale_f32_16x16x128_f8f6f4 v[96:99], v[8:15], v[36:43], v[96:99], v198, v198 op_sel_hi:[0,0,0]
	v_mfma_scale_f32_16x16x128_f8f6f4 v[92:95], v[0:7], v[36:43], v[92:95], v198, v198 op_sel_hi:[0,0,0]
	v_mfma_scale_f32_16x16x128_f8f6f4 v[88:91], v[8:15], v[44:51], v[88:91], v198, v198 op_sel_hi:[0,0,0]
	v_mfma_scale_f32_16x16x128_f8f6f4 v[84:87], v[0:7], v[44:51], v[84:87], v198, v198 op_sel_hi:[0,0,0]
	v_mfma_scale_f32_16x16x128_f8f6f4 v[80:83], v[8:15], v[52:59], v[80:83], v198, v198 op_sel_hi:[0,0,0]
	v_mfma_scale_f32_16x16x128_f8f6f4 v[76:79], v[0:7], v[52:59], v[76:79], v198, v198 op_sel_hi:[0,0,0]
	v_mfma_scale_f32_16x16x128_f8f6f4 v[72:75], v[8:15], v[218:225], v[72:75], v198, v198 op_sel_hi:[0,0,0]
	v_mfma_scale_f32_16x16x128_f8f6f4 v[68:71], v[0:7], v[218:225], v[68:71], v198, v198 op_sel_hi:[0,0,0]
	s_setprio 0
	s_barrier
	ds_read_b128 v[24:27], v202 offset:0x8000
	ds_read_b128 v[28:31], v202 offset:0x8400
	ds_read_b128 v[16:19], v202 offset:0x8800
	ds_read_b128 v[20:23], v202 offset:0x8c00
	ds_read_b128 v[36:39], v201 offset:0x8000
	ds_read_b128 v[40:43], v201 offset:0x8400
	ds_read_b128 v[44:47], v201 offset:0x8800
	ds_read_b128 v[48:51], v201 offset:0x8c00
	ds_read_b128 v[52:55], v201 offset:0x9000
	ds_read_b128 v[56:59], v201 offset:0x9400
	ds_read_b128 v[218:221], v201 offset:0x9800
	ds_read_b128 v[222:225], v201 offset:0x9c00
	ds_read_b128 v[8:11], v202 offset:0xc000
	ds_read_b128 v[12:15], v202 offset:0xc400
	ds_read_b128 v[0:3], v202 offset:0xc800
	ds_read_b128 v[4:7], v202 offset:0xcc00
	s_mov_b32 m0, s50
	v_cndmask_b32_e32 v62, v207, v34, vcc
	buffer_load_dwordx4 v62, s[4:7], s67 offen lds
	v_cndmask_b32_e32 v62, v206, v35, vcc
	s_mov_b32 m0, s51
	s_nop 0
	buffer_load_dwordx4 v62, s[4:7], s67 offen lds
	s_waitcnt vmcnt(8)
	s_waitcnt lgkmcnt(0)
	s_barrier
	s_setprio 1
	v_mfma_scale_f32_16x16x128_f8f6f4 v[192:195], v[24:31], v[36:43], v[192:195], v198, v198 op_sel_hi:[0,0,0]
	v_mfma_scale_f32_16x16x128_f8f6f4 v[188:191], v[16:23], v[36:43], v[188:191], v198, v198 op_sel_hi:[0,0,0]
	v_mfma_scale_f32_16x16x128_f8f6f4 v[184:187], v[24:31], v[44:51], v[184:187], v198, v198 op_sel_hi:[0,0,0]
	v_mfma_scale_f32_16x16x128_f8f6f4 v[180:183], v[16:23], v[44:51], v[180:183], v198, v198 op_sel_hi:[0,0,0]
	v_mfma_scale_f32_16x16x128_f8f6f4 v[176:179], v[24:31], v[52:59], v[176:179], v198, v198 op_sel_hi:[0,0,0]
	v_mfma_scale_f32_16x16x128_f8f6f4 v[172:175], v[16:23], v[52:59], v[172:175], v198, v198 op_sel_hi:[0,0,0]
	v_mfma_scale_f32_16x16x128_f8f6f4 v[168:171], v[24:31], v[218:225], v[168:171], v198, v198 op_sel_hi:[0,0,0]
	v_mfma_scale_f32_16x16x128_f8f6f4 v[164:167], v[16:23], v[218:225], v[164:167], v198, v198 op_sel_hi:[0,0,0]
	s_setprio 0
	s_setprio 1
	v_mfma_scale_f32_16x16x128_f8f6f4 v[160:163], v[8:15], v[36:43], v[160:163], v198, v198 op_sel_hi:[0,0,0]
	v_mfma_scale_f32_16x16x128_f8f6f4 v[156:159], v[0:7], v[36:43], v[156:159], v198, v198 op_sel_hi:[0,0,0]
	v_mfma_scale_f32_16x16x128_f8f6f4 v[152:155], v[8:15], v[44:51], v[152:155], v198, v198 op_sel_hi:[0,0,0]
	v_mfma_scale_f32_16x16x128_f8f6f4 v[148:151], v[0:7], v[44:51], v[148:151], v198, v198 op_sel_hi:[0,0,0]
	v_mfma_scale_f32_16x16x128_f8f6f4 v[144:147], v[8:15], v[52:59], v[144:147], v198, v198 op_sel_hi:[0,0,0]
	v_mfma_scale_f32_16x16x128_f8f6f4 v[140:143], v[0:7], v[52:59], v[140:143], v198, v198 op_sel_hi:[0,0,0]
	v_mfma_scale_f32_16x16x128_f8f6f4 v[136:139], v[8:15], v[218:225], v[136:139], v198, v198 op_sel_hi:[0,0,0]
	v_mfma_scale_f32_16x16x128_f8f6f4 v[132:135], v[0:7], v[218:225], v[132:135], v198, v198 op_sel_hi:[0,0,0]
	s_setprio 0
	s_barrier
	ds_read_b128 v[36:39], v201 offset:0xc000
	ds_read_b128 v[40:43], v201 offset:0xc400
	ds_read_b128 v[44:47], v201 offset:0xc800
	ds_read_b128 v[48:51], v201 offset:0xcc00
	ds_read_b128 v[52:55], v201 offset:0xd000
	ds_read_b128 v[56:59], v201 offset:0xd400
	ds_read_b128 v[218:221], v201 offset:0xd800
	ds_read_b128 v[222:225], v201 offset:0xdc00
	s_mov_b32 m0, s64
	s_add_i32 s67, s66, 0x80
	buffer_load_dwordx4 v200, s[8:11], s67 offen lds
	s_add_i32 s67, s66, 0x80080
	s_mov_b32 m0, s65
	s_nop 0
	buffer_load_dwordx4 v200, s[8:11], s67 offen lds
	s_add_i32 s67, s66, 0x8080
	s_mov_b32 m0, s70
	s_add_i32 s66, s66, 0x88080
	buffer_load_dwordx4 v200, s[8:11], s67 offen lds
	s_mov_b32 m0, s71
	s_nop 0
	buffer_load_dwordx4 v200, s[8:11], s66 offen lds
	s_mov_b32 m0, s68
	s_nop 0
	buffer_load_dwordx4 v60, s[4:7], s61 offen lds
	s_mov_b32 m0, s69
	s_nop 0
	buffer_load_dwordx4 v61, s[4:7], s61 offen lds
	s_waitcnt vmcnt(8)
	s_waitcnt lgkmcnt(0)
	s_barrier
	s_setprio 1
	v_mfma_scale_f32_16x16x128_f8f6f4 v[128:131], v[24:31], v[36:43], v[128:131], v198, v198 op_sel_hi:[0,0,0]
	v_mfma_scale_f32_16x16x128_f8f6f4 v[124:127], v[16:23], v[36:43], v[124:127], v198, v198 op_sel_hi:[0,0,0]
	v_mfma_scale_f32_16x16x128_f8f6f4 v[120:123], v[24:31], v[44:51], v[120:123], v198, v198 op_sel_hi:[0,0,0]
	v_mfma_scale_f32_16x16x128_f8f6f4 v[116:119], v[16:23], v[44:51], v[116:119], v198, v198 op_sel_hi:[0,0,0]
	v_mfma_scale_f32_16x16x128_f8f6f4 v[112:115], v[24:31], v[52:59], v[112:115], v198, v198 op_sel_hi:[0,0,0]
	v_mfma_scale_f32_16x16x128_f8f6f4 v[108:111], v[16:23], v[52:59], v[108:111], v198, v198 op_sel_hi:[0,0,0]
	v_mfma_scale_f32_16x16x128_f8f6f4 v[104:107], v[24:31], v[218:225], v[104:107], v198, v198 op_sel_hi:[0,0,0]
	v_mfma_scale_f32_16x16x128_f8f6f4 v[100:103], v[16:23], v[218:225], v[100:103], v198, v198 op_sel_hi:[0,0,0]
	s_setprio 0
	s_setprio 1
	v_mfma_scale_f32_16x16x128_f8f6f4 v[96:99], v[8:15], v[36:43], v[96:99], v198, v198 op_sel_hi:[0,0,0]
	v_mfma_scale_f32_16x16x128_f8f6f4 v[92:95], v[0:7], v[36:43], v[92:95], v198, v198 op_sel_hi:[0,0,0]
	v_mfma_scale_f32_16x16x128_f8f6f4 v[88:91], v[8:15], v[44:51], v[88:91], v198, v198 op_sel_hi:[0,0,0]
	v_mfma_scale_f32_16x16x128_f8f6f4 v[84:87], v[0:7], v[44:51], v[84:87], v198, v198 op_sel_hi:[0,0,0]
	v_mfma_scale_f32_16x16x128_f8f6f4 v[80:83], v[8:15], v[52:59], v[80:83], v198, v198 op_sel_hi:[0,0,0]
	v_mfma_scale_f32_16x16x128_f8f6f4 v[76:79], v[0:7], v[52:59], v[76:79], v198, v198 op_sel_hi:[0,0,0]
	v_mfma_scale_f32_16x16x128_f8f6f4 v[72:75], v[8:15], v[218:225], v[72:75], v198, v198 op_sel_hi:[0,0,0]
	v_mfma_scale_f32_16x16x128_f8f6f4 v[68:71], v[0:7], v[218:225], v[68:71], v198, v198 op_sel_hi:[0,0,0]
	s_setprio 0
	s_barrier
	s_add_i32 s37, s37, 2
	s_addk_i32 s36, 0x100
	s_addk_i32 s33, 0x100
	s_cmp_gt_u32 s37, 29
	s_cbranch_scc0 .LBB0_1330
	s_and_b64 vcc, exec, s[28:29]
	s_cbranch_vccz .LBB0_1333
	s_barrier

.LBB0_1369:
	s_add_i32 s33, s88, 0x180
	s_add_i32 s40, s89, 0x180
	s_waitcnt lgkmcnt(0)
	s_barrier
	s_setprio 1
	v_mfma_scale_f32_16x16x128_f8f6f4 v[128:131], v[24:31], v[56:63], 0, v235, v235 op_sel_hi:[0,0,0]
	v_mfma_scale_f32_16x16x128_f8f6f4 v[124:127], v[16:23], v[56:63], 0, v235, v235 op_sel_hi:[0,0,0]
	v_mfma_scale_f32_16x16x128_f8f6f4 v[120:123], v[24:31], v[48:55], 0, v235, v235 op_sel_hi:[0,0,0]
	v_mfma_scale_f32_16x16x128_f8f6f4 v[116:119], v[16:23], v[48:55], 0, v235, v235 op_sel_hi:[0,0,0]
	v_mfma_scale_f32_16x16x128_f8f6f4 v[112:115], v[24:31], v[40:47], 0, v235, v235 op_sel_hi:[0,0,0]
	v_mfma_scale_f32_16x16x128_f8f6f4 v[108:111], v[16:23], v[40:47], 0, v235, v235 op_sel_hi:[0,0,0]
	v_mfma_scale_f32_16x16x128_f8f6f4 v[104:107], v[24:31], v[32:39], 0, v235, v235 op_sel_hi:[0,0,0]
	v_mfma_scale_f32_16x16x128_f8f6f4 v[100:103], v[16:23], v[32:39], 0, v235, v235 op_sel_hi:[0,0,0]
	s_setprio 0
	s_setprio 1
	v_mfma_scale_f32_16x16x128_f8f6f4 v[96:99], v[8:15], v[56:63], 0, v235, v235 op_sel_hi:[0,0,0]
	v_mfma_scale_f32_16x16x128_f8f6f4 v[92:95], v[0:7], v[56:63], 0, v235, v235 op_sel_hi:[0,0,0]
	v_mfma_scale_f32_16x16x128_f8f6f4 v[88:91], v[8:15], v[48:55], 0, v235, v235 op_sel_hi:[0,0,0]
	v_mfma_scale_f32_16x16x128_f8f6f4 v[84:87], v[0:7], v[48:55], 0, v235, v235 op_sel_hi:[0,0,0]
	v_mfma_scale_f32_16x16x128_f8f6f4 v[80:83], v[8:15], v[40:47], 0, v235, v235 op_sel_hi:[0,0,0]
	v_mfma_scale_f32_16x16x128_f8f6f4 v[76:79], v[0:7], v[40:47], 0, v235, v235 op_sel_hi:[0,0,0]
	v_mfma_scale_f32_16x16x128_f8f6f4 v[72:75], v[8:15], v[32:39], 0, v235, v235 op_sel_hi:[0,0,0]
	v_mfma_scale_f32_16x16x128_f8f6f4 v[68:71], v[0:7], v[32:39], 0, v235, v235 op_sel_hi:[0,0,0]
	s_setprio 0
	s_barrier
	ds_read_b128 v[16:19], v233 offset:0x8000
	ds_read_b128 v[20:23], v233 offset:0x8400
	ds_read_b128 v[24:27], v233 offset:0x8800
	ds_read_b128 v[28:31], v233 offset:0x8c00
	ds_read_b128 v[32:35], v232 offset:0x8000
	ds_read_b128 v[36:39], v232 offset:0x8400
	ds_read_b128 v[40:43], v232 offset:0x8800
	ds_read_b128 v[44:47], v232 offset:0x8c00
	ds_read_b128 v[48:51], v232 offset:0x9000
	ds_read_b128 v[52:55], v232 offset:0x9400
	ds_read_b128 v[56:59], v232 offset:0x9800
	ds_read_b128 v[60:63], v232 offset:0x9c00
	ds_read_b128 v[8:11], v233 offset:0xc000
	ds_read_b128 v[12:15], v233 offset:0xc400
	ds_read_b128 v[0:3], v233 offset:0xc800
	ds_read_b128 v[4:7], v233 offset:0xcc00
	s_mov_b32 m0, s62
	s_add_i32 s10, s88, 0x10100
	buffer_load_dwordx4 v230, s[4:7], s10 offen lds
	s_add_i32 s10, s88, 0x18100
	s_mov_b32 m0, s63
	s_nop 0
	buffer_load_dwordx4 v230, s[4:7], s10 offen lds
	s_waitcnt vmcnt(8)
	s_waitcnt lgkmcnt(0)
	s_barrier
	s_setprio 1
	v_mfma_scale_f32_16x16x128_f8f6f4 v[192:195], v[16:23], v[32:39], v[192:195], v235, v235 op_sel_hi:[0,0,0]
	v_mfma_scale_f32_16x16x128_f8f6f4 v[188:191], v[24:31], v[32:39], v[188:191], v235, v235 op_sel_hi:[0,0,0]
	v_mfma_scale_f32_16x16x128_f8f6f4 v[184:187], v[16:23], v[40:47], v[184:187], v235, v235 op_sel_hi:[0,0,0]
	v_mfma_scale_f32_16x16x128_f8f6f4 v[180:183], v[24:31], v[40:47], v[180:183], v235, v235 op_sel_hi:[0,0,0]
	v_mfma_scale_f32_16x16x128_f8f6f4 v[176:179], v[16:23], v[48:55], v[176:179], v235, v235 op_sel_hi:[0,0,0]
	v_mfma_scale_f32_16x16x128_f8f6f4 v[172:175], v[24:31], v[48:55], v[172:175], v235, v235 op_sel_hi:[0,0,0]
	v_mfma_scale_f32_16x16x128_f8f6f4 v[168:171], v[16:23], v[56:63], v[168:171], v235, v235 op_sel_hi:[0,0,0]
	v_mfma_scale_f32_16x16x128_f8f6f4 v[164:167], v[24:31], v[56:63], v[164:167], v235, v235 op_sel_hi:[0,0,0]
	s_setprio 0
	s_setprio 1
	v_mfma_scale_f32_16x16x128_f8f6f4 v[160:163], v[8:15], v[32:39], v[160:163], v235, v235 op_sel_hi:[0,0,0]
	v_mfma_scale_f32_16x16x128_f8f6f4 v[156:159], v[0:7], v[32:39], v[156:159], v235, v235 op_sel_hi:[0,0,0]
	v_mfma_scale_f32_16x16x128_f8f6f4 v[152:155], v[8:15], v[40:47], v[152:155], v235, v235 op_sel_hi:[0,0,0]
	v_mfma_scale_f32_16x16x128_f8f6f4 v[148:151], v[0:7], v[40:47], v[148:151], v235, v235 op_sel_hi:[0,0,0]
	v_mfma_scale_f32_16x16x128_f8f6f4 v[144:147], v[8:15], v[48:55], v[144:147], v235, v235 op_sel_hi:[0,0,0]
	v_mfma_scale_f32_16x16x128_f8f6f4 v[140:143], v[0:7], v[48:55], v[140:143], v235, v235 op_sel_hi:[0,0,0]
	v_mfma_scale_f32_16x16x128_f8f6f4 v[136:139], v[8:15], v[56:63], v[136:139], v235, v235 op_sel_hi:[0,0,0]
	v_mfma_scale_f32_16x16x128_f8f6f4 v[132:135], v[0:7], v[56:63], v[132:135], v235, v235 op_sel_hi:[0,0,0]
	s_setprio 0
	s_barrier
	ds_read_b128 v[32:35], v232 offset:0xc000
	ds_read_b128 v[36:39], v232 offset:0xc400
	ds_read_b128 v[40:43], v232 offset:0xc800
	ds_read_b128 v[44:47], v232 offset:0xcc00
	ds_read_b128 v[48:51], v232 offset:0xd000
	ds_read_b128 v[52:55], v232 offset:0xd400
	ds_read_b128 v[56:59], v232 offset:0xd800
	ds_read_b128 v[60:63], v232 offset:0xdc00
	s_mov_b32 m0, s64
	s_mov_b32 s10, s6
	s_mov_b32 s11, s7
	buffer_load_dwordx4 v231, s[8:11], s40 offen lds
	s_add_i32 s40, s89, 0x10180
	s_mov_b32 m0, s65
	s_nop 0
	buffer_load_dwordx4 v231, s[8:11], s40 offen lds
	s_add_i32 s40, s89, 0x1180
	s_mov_b32 m0, s70
	s_nop 0
	buffer_load_dwordx4 v231, s[8:11], s40 offen lds
	s_add_i32 s40, s89, 0x11180
	s_mov_b32 m0, s71
	s_nop 0
	buffer_load_dwordx4 v231, s[8:11], s40 offen lds
	s_mov_b32 m0, s68
	s_nop 0
	buffer_load_dwordx4 v230, s[4:7], s33 offen lds
	s_add_i32 s33, s88, 0x8180
	s_mov_b32 m0, s69
	s_nop 0
	buffer_load_dwordx4 v230, s[4:7], s33 offen lds
	s_waitcnt vmcnt(8)
	s_waitcnt lgkmcnt(0)
	s_barrier
	s_setprio 1
	v_mfma_scale_f32_16x16x128_f8f6f4 v[128:131], v[16:23], v[32:39], v[128:131], v235, v235 op_sel_hi:[0,0,0]
	v_mfma_scale_f32_16x16x128_f8f6f4 v[124:127], v[24:31], v[32:39], v[124:127], v235, v235 op_sel_hi:[0,0,0]
	v_mfma_scale_f32_16x16x128_f8f6f4 v[120:123], v[16:23], v[40:47], v[120:123], v235, v235 op_sel_hi:[0,0,0]
	v_mfma_scale_f32_16x16x128_f8f6f4 v[116:119], v[24:31], v[40:47], v[116:119], v235, v235 op_sel_hi:[0,0,0]
	v_mfma_scale_f32_16x16x128_f8f6f4 v[112:115], v[16:23], v[48:55], v[112:115], v235, v235 op_sel_hi:[0,0,0]
	v_mfma_scale_f32_16x16x128_f8f6f4 v[108:111], v[24:31], v[48:55], v[108:111], v235, v235 op_sel_hi:[0,0,0]
	v_mfma_scale_f32_16x16x128_f8f6f4 v[104:107], v[16:23], v[56:63], v[104:107], v235, v235 op_sel_hi:[0,0,0]
	v_mfma_scale_f32_16x16x128_f8f6f4 v[100:103], v[24:31], v[56:63], v[100:103], v235, v235 op_sel_hi:[0,0,0]
	s_setprio 0
	s_setprio 1
	v_mfma_scale_f32_16x16x128_f8f6f4 v[96:99], v[8:15], v[32:39], v[96:99], v235, v235 op_sel_hi:[0,0,0]
	v_mfma_scale_f32_16x16x128_f8f6f4 v[92:95], v[0:7], v[32:39], v[92:95], v235, v235 op_sel_hi:[0,0,0]
	v_mfma_scale_f32_16x16x128_f8f6f4 v[88:91], v[8:15], v[40:47], v[88:91], v235, v235 op_sel_hi:[0,0,0]
	v_mfma_scale_f32_16x16x128_f8f6f4 v[84:87], v[0:7], v[40:47], v[84:87], v235, v235 op_sel_hi:[0,0,0]
	v_mfma_scale_f32_16x16x128_f8f6f4 v[80:83], v[8:15], v[48:55], v[80:83], v235, v235 op_sel_hi:[0,0,0]
	v_mfma_scale_f32_16x16x128_f8f6f4 v[76:79], v[0:7], v[48:55], v[76:79], v235, v235 op_sel_hi:[0,0,0]
	v_mfma_scale_f32_16x16x128_f8f6f4 v[72:75], v[8:15], v[56:63], v[72:75], v235, v235 op_sel_hi:[0,0,0]
	v_mfma_scale_f32_16x16x128_f8f6f4 v[68:71], v[0:7], v[56:63], v[68:71], v235, v235 op_sel_hi:[0,0,0]
	s_setprio 0
	s_barrier
	ds_read_b128 v[16:19], v233 offset:0
	ds_read_b128 v[20:23], v233 offset:0x400
	ds_read_b128 v[24:27], v233 offset:0x800
	ds_read_b128 v[28:31], v233 offset:0xc00
	ds_read_b128 v[32:35], v232 offset:0
	ds_read_b128 v[36:39], v232 offset:0x400
	ds_read_b128 v[40:43], v232 offset:0x800
	ds_read_b128 v[44:47], v232 offset:0xc00
	ds_read_b128 v[48:51], v232 offset:0x1000
	ds_read_b128 v[52:55], v232 offset:0x1400
	ds_read_b128 v[56:59], v232 offset:0x1800
	ds_read_b128 v[60:63], v232 offset:0x1c00
	ds_read_b128 v[8:11], v233 offset:0x4000
	ds_read_b128 v[12:15], v233 offset:0x4400
	ds_read_b128 v[0:3], v233 offset:0x4800
	ds_read_b128 v[4:7], v233 offset:0x4c00
	s_add_i32 s33, s85, 0x80
	s_mov_b32 m0, s74
	s_add_i32 s40, s88, 0x10180
	buffer_load_dwordx4 v230, s[4:7], s40 offen lds
	s_add_i32 s40, s88, 0x18180
	s_mov_b32 m0, s76
	s_nop 0
	buffer_load_dwordx4 v230, s[4:7], s40 offen lds
	s_waitcnt vmcnt(8)
	s_waitcnt lgkmcnt(0)
	s_barrier
	s_setprio 1
	v_mfma_scale_f32_16x16x128_f8f6f4 v[192:195], v[16:23], v[32:39], v[192:195], v235, v235 op_sel_hi:[0,0,0]
	v_mfma_scale_f32_16x16x128_f8f6f4 v[188:191], v[24:31], v[32:39], v[188:191], v235, v235 op_sel_hi:[0,0,0]
	v_mfma_scale_f32_16x16x128_f8f6f4 v[184:187], v[16:23], v[40:47], v[184:187], v235, v235 op_sel_hi:[0,0,0]
	v_mfma_scale_f32_16x16x128_f8f6f4 v[180:183], v[24:31], v[40:47], v[180:183], v235, v235 op_sel_hi:[0,0,0]
	v_mfma_scale_f32_16x16x128_f8f6f4 v[176:179], v[16:23], v[48:55], v[176:179], v235, v235 op_sel_hi:[0,0,0]
	v_mfma_scale_f32_16x16x128_f8f6f4 v[172:175], v[24:31], v[48:55], v[172:175], v235, v235 op_sel_hi:[0,0,0]
	v_mfma_scale_f32_16x16x128_f8f6f4 v[168:171], v[16:23], v[56:63], v[168:171], v235, v235 op_sel_hi:[0,0,0]
	v_mfma_scale_f32_16x16x128_f8f6f4 v[164:167], v[24:31], v[56:63], v[164:167], v235, v235 op_sel_hi:[0,0,0]
	s_setprio 0
	s_setprio 1
	v_mfma_scale_f32_16x16x128_f8f6f4 v[160:163], v[8:15], v[32:39], v[160:163], v235, v235 op_sel_hi:[0,0,0]
	v_mfma_scale_f32_16x16x128_f8f6f4 v[156:159], v[0:7], v[32:39], v[156:159], v235, v235 op_sel_hi:[0,0,0]
	v_mfma_scale_f32_16x16x128_f8f6f4 v[152:155], v[8:15], v[40:47], v[152:155], v235, v235 op_sel_hi:[0,0,0]
	v_mfma_scale_f32_16x16x128_f8f6f4 v[148:151], v[0:7], v[40:47], v[148:151], v235, v235 op_sel_hi:[0,0,0]
	v_mfma_scale_f32_16x16x128_f8f6f4 v[144:147], v[8:15], v[48:55], v[144:147], v235, v235 op_sel_hi:[0,0,0]
	v_mfma_scale_f32_16x16x128_f8f6f4 v[140:143], v[0:7], v[48:55], v[140:143], v235, v235 op_sel_hi:[0,0,0]
	v_mfma_scale_f32_16x16x128_f8f6f4 v[136:139], v[8:15], v[56:63], v[136:139], v235, v235 op_sel_hi:[0,0,0]
	v_mfma_scale_f32_16x16x128_f8f6f4 v[132:135], v[0:7], v[56:63], v[132:135], v235, v235 op_sel_hi:[0,0,0]
	s_setprio 0
	s_barrier
	ds_read_b128 v[32:35], v232 offset:0x4000
	ds_read_b128 v[36:39], v232 offset:0x4400
	ds_read_b128 v[40:43], v232 offset:0x4800
	ds_read_b128 v[44:47], v232 offset:0x4c00
	ds_read_b128 v[48:51], v232 offset:0x5000
	ds_read_b128 v[52:55], v232 offset:0x5400
	ds_read_b128 v[56:59], v232 offset:0x5800
	ds_read_b128 v[60:63], v232 offset:0x5c00
	s_mov_b32 m0, s46
	s_nop 0
	buffer_load_dwordx4 v231, s[8:11], s86 offen lds
	s_add_i32 s40, s86, 0x10000
	s_mov_b32 m0, s47
	s_nop 0
	buffer_load_dwordx4 v231, s[8:11], s40 offen lds
	s_add_i32 s40, s86, 0x1000
	s_mov_b32 m0, s49
	s_nop 0
	buffer_load_dwordx4 v231, s[8:11], s40 offen lds
	s_add_i32 s40, s86, 0x11000
	s_mov_b32 m0, s50
	s_nop 0
	buffer_load_dwordx4 v231, s[8:11], s40 offen lds
	s_mov_b32 m0, s48
	s_add_i32 s40, s85, 0x8000
	buffer_load_dwordx4 v230, s[4:7], s85 offen lds
	s_mov_b32 m0, s51
	s_nop 0
	buffer_load_dwordx4 v230, s[4:7], s40 offen lds
	s_waitcnt vmcnt(8)
	s_waitcnt lgkmcnt(0)
	s_barrier
	s_setprio 1
	v_mfma_scale_f32_16x16x128_f8f6f4 v[128:131], v[16:23], v[32:39], v[128:131], v235, v235 op_sel_hi:[0,0,0]
	v_mfma_scale_f32_16x16x128_f8f6f4 v[124:127], v[24:31], v[32:39], v[124:127], v235, v235 op_sel_hi:[0,0,0]
	v_mfma_scale_f32_16x16x128_f8f6f4 v[120:123], v[16:23], v[40:47], v[120:123], v235, v235 op_sel_hi:[0,0,0]
	v_mfma_scale_f32_16x16x128_f8f6f4 v[116:119], v[24:31], v[40:47], v[116:119], v235, v235 op_sel_hi:[0,0,0]
	v_mfma_scale_f32_16x16x128_f8f6f4 v[112:115], v[16:23], v[48:55], v[112:115], v235, v235 op_sel_hi:[0,0,0]
	v_mfma_scale_f32_16x16x128_f8f6f4 v[108:111], v[24:31], v[48:55], v[108:111], v235, v235 op_sel_hi:[0,0,0]
	v_mfma_scale_f32_16x16x128_f8f6f4 v[104:107], v[16:23], v[56:63], v[104:107], v235, v235 op_sel_hi:[0,0,0]
	v_mfma_scale_f32_16x16x128_f8f6f4 v[100:103], v[24:31], v[56:63], v[100:103], v235, v235 op_sel_hi:[0,0,0]
	s_setprio 0
	s_setprio 1
	v_mfma_scale_f32_16x16x128_f8f6f4 v[96:99], v[8:15], v[32:39], v[96:99], v235, v235 op_sel_hi:[0,0,0]
	v_mfma_scale_f32_16x16x128_f8f6f4 v[92:95], v[0:7], v[32:39], v[92:95], v235, v235 op_sel_hi:[0,0,0]
	v_mfma_scale_f32_16x16x128_f8f6f4 v[88:91], v[8:15], v[40:47], v[88:91], v235, v235 op_sel_hi:[0,0,0]
	v_mfma_scale_f32_16x16x128_f8f6f4 v[84:87], v[0:7], v[40:47], v[84:87], v235, v235 op_sel_hi:[0,0,0]
	v_mfma_scale_f32_16x16x128_f8f6f4 v[80:83], v[8:15], v[48:55], v[80:83], v235, v235 op_sel_hi:[0,0,0]
	v_mfma_scale_f32_16x16x128_f8f6f4 v[76:79], v[0:7], v[48:55], v[76:79], v235, v235 op_sel_hi:[0,0,0]
	v_mfma_scale_f32_16x16x128_f8f6f4 v[72:75], v[8:15], v[56:63], v[72:75], v235, v235 op_sel_hi:[0,0,0]
	v_mfma_scale_f32_16x16x128_f8f6f4 v[68:71], v[0:7], v[56:63], v[68:71], v235, v235 op_sel_hi:[0,0,0]
	s_setprio 0
	s_barrier
	ds_read_b128 v[16:19], v233 offset:0x8000
	ds_read_b128 v[20:23], v233 offset:0x8400
	ds_read_b128 v[24:27], v233 offset:0x8800
	ds_read_b128 v[28:31], v233 offset:0x8c00
	ds_read_b128 v[32:35], v232 offset:0x8000
	ds_read_b128 v[36:39], v232 offset:0x8400
	ds_read_b128 v[40:43], v232 offset:0x8800
	ds_read_b128 v[44:47], v232 offset:0x8c00
	ds_read_b128 v[48:51], v232 offset:0x9000
	ds_read_b128 v[52:55], v232 offset:0x9400
	ds_read_b128 v[56:59], v232 offset:0x9800
	ds_read_b128 v[60:63], v232 offset:0x9c00
	ds_read_b128 v[8:11], v233 offset:0xc000
	ds_read_b128 v[12:15], v233 offset:0xc400
	ds_read_b128 v[0:3], v233 offset:0xc800
	ds_read_b128 v[4:7], v233 offset:0xcc00
	s_mov_b32 m0, s62
	s_add_i32 s40, s85, 0x10000
	buffer_load_dwordx4 v230, s[4:7], s40 offen lds
	s_add_i32 s40, s85, 0x18000
	s_mov_b32 m0, s63
	s_nop 0
	buffer_load_dwordx4 v230, s[4:7], s40 offen lds
	s_waitcnt vmcnt(8)
	s_waitcnt lgkmcnt(0)
	s_barrier
	s_setprio 1
	v_mfma_scale_f32_16x16x128_f8f6f4 v[192:195], v[16:23], v[32:39], v[192:195], v235, v235 op_sel_hi:[0,0,0]
	v_mfma_scale_f32_16x16x128_f8f6f4 v[188:191], v[24:31], v[32:39], v[188:191], v235, v235 op_sel_hi:[0,0,0]
	v_mfma_scale_f32_16x16x128_f8f6f4 v[184:187], v[16:23], v[40:47], v[184:187], v235, v235 op_sel_hi:[0,0,0]
	v_mfma_scale_f32_16x16x128_f8f6f4 v[180:183], v[24:31], v[40:47], v[180:183], v235, v235 op_sel_hi:[0,0,0]
	v_mfma_scale_f32_16x16x128_f8f6f4 v[176:179], v[16:23], v[48:55], v[176:179], v235, v235 op_sel_hi:[0,0,0]
	v_mfma_scale_f32_16x16x128_f8f6f4 v[172:175], v[24:31], v[48:55], v[172:175], v235, v235 op_sel_hi:[0,0,0]
	v_mfma_scale_f32_16x16x128_f8f6f4 v[168:171], v[16:23], v[56:63], v[168:171], v235, v235 op_sel_hi:[0,0,0]
	v_mfma_scale_f32_16x16x128_f8f6f4 v[164:167], v[24:31], v[56:63], v[164:167], v235, v235 op_sel_hi:[0,0,0]
	s_setprio 0
	s_setprio 1
	v_mfma_scale_f32_16x16x128_f8f6f4 v[160:163], v[8:15], v[32:39], v[160:163], v235, v235 op_sel_hi:[0,0,0]
	v_mfma_scale_f32_16x16x128_f8f6f4 v[156:159], v[0:7], v[32:39], v[156:159], v235, v235 op_sel_hi:[0,0,0]
	v_mfma_scale_f32_16x16x128_f8f6f4 v[152:155], v[8:15], v[40:47], v[152:155], v235, v235 op_sel_hi:[0,0,0]
	v_mfma_scale_f32_16x16x128_f8f6f4 v[148:151], v[0:7], v[40:47], v[148:151], v235, v235 op_sel_hi:[0,0,0]
	v_mfma_scale_f32_16x16x128_f8f6f4 v[144:147], v[8:15], v[48:55], v[144:147], v235, v235 op_sel_hi:[0,0,0]
	v_mfma_scale_f32_16x16x128_f8f6f4 v[140:143], v[0:7], v[48:55], v[140:143], v235, v235 op_sel_hi:[0,0,0]
	v_mfma_scale_f32_16x16x128_f8f6f4 v[136:139], v[8:15], v[56:63], v[136:139], v235, v235 op_sel_hi:[0,0,0]
	v_mfma_scale_f32_16x16x128_f8f6f4 v[132:135], v[0:7], v[56:63], v[132:135], v235, v235 op_sel_hi:[0,0,0]
	s_setprio 0
	s_barrier
	ds_read_b128 v[32:35], v232 offset:0xc000
	ds_read_b128 v[36:39], v232 offset:0xc400
	ds_read_b128 v[40:43], v232 offset:0xc800
	ds_read_b128 v[44:47], v232 offset:0xcc00
	ds_read_b128 v[48:51], v232 offset:0xd000
	ds_read_b128 v[52:55], v232 offset:0xd400
	ds_read_b128 v[56:59], v232 offset:0xd800
	ds_read_b128 v[60:63], v232 offset:0xdc00
	s_mov_b32 m0, s64
	s_add_i32 s40, s86, 0x80
	buffer_load_dwordx4 v231, s[8:11], s40 offen lds
	s_add_i32 s40, s86, 0x10080
	s_mov_b32 m0, s65
	s_nop 0
	buffer_load_dwordx4 v231, s[8:11], s40 offen lds
	s_add_i32 s40, s86, 0x1080
	s_mov_b32 m0, s70
	s_nop 0
	buffer_load_dwordx4 v231, s[8:11], s40 offen lds
	s_add_i32 s40, s86, 0x11080
	s_mov_b32 m0, s71
	s_nop 0
	buffer_load_dwordx4 v231, s[8:11], s40 offen lds
	s_mov_b32 m0, s68
	s_add_i32 s10, s85, 0x8080
	buffer_load_dwordx4 v230, s[4:7], s33 offen lds
	s_mov_b32 m0, s69
	s_nop 0
	buffer_load_dwordx4 v230, s[4:7], s10 offen lds
	s_waitcnt vmcnt(8)
	s_waitcnt lgkmcnt(0)
	s_barrier
	s_setprio 1
	v_mfma_scale_f32_16x16x128_f8f6f4 v[128:131], v[16:23], v[32:39], v[128:131], v235, v235 op_sel_hi:[0,0,0]
	v_mfma_scale_f32_16x16x128_f8f6f4 v[124:127], v[24:31], v[32:39], v[124:127], v235, v235 op_sel_hi:[0,0,0]
	v_mfma_scale_f32_16x16x128_f8f6f4 v[120:123], v[16:23], v[40:47], v[120:123], v235, v235 op_sel_hi:[0,0,0]
	v_mfma_scale_f32_16x16x128_f8f6f4 v[116:119], v[24:31], v[40:47], v[116:119], v235, v235 op_sel_hi:[0,0,0]
	v_mfma_scale_f32_16x16x128_f8f6f4 v[112:115], v[16:23], v[48:55], v[112:115], v235, v235 op_sel_hi:[0,0,0]
	v_mfma_scale_f32_16x16x128_f8f6f4 v[108:111], v[24:31], v[48:55], v[108:111], v235, v235 op_sel_hi:[0,0,0]
	v_mfma_scale_f32_16x16x128_f8f6f4 v[104:107], v[16:23], v[56:63], v[104:107], v235, v235 op_sel_hi:[0,0,0]
	v_mfma_scale_f32_16x16x128_f8f6f4 v[100:103], v[24:31], v[56:63], v[100:103], v235, v235 op_sel_hi:[0,0,0]
	s_setprio 0
	s_setprio 1
	v_mfma_scale_f32_16x16x128_f8f6f4 v[96:99], v[8:15], v[32:39], v[96:99], v235, v235 op_sel_hi:[0,0,0]
	v_mfma_scale_f32_16x16x128_f8f6f4 v[92:95], v[0:7], v[32:39], v[92:95], v235, v235 op_sel_hi:[0,0,0]
	v_mfma_scale_f32_16x16x128_f8f6f4 v[88:91], v[8:15], v[40:47], v[88:91], v235, v235 op_sel_hi:[0,0,0]
	v_mfma_scale_f32_16x16x128_f8f6f4 v[84:87], v[0:7], v[40:47], v[84:87], v235, v235 op_sel_hi:[0,0,0]
	v_mfma_scale_f32_16x16x128_f8f6f4 v[80:83], v[8:15], v[48:55], v[80:83], v235, v235 op_sel_hi:[0,0,0]
	v_mfma_scale_f32_16x16x128_f8f6f4 v[76:79], v[0:7], v[48:55], v[76:79], v235, v235 op_sel_hi:[0,0,0]
	v_mfma_scale_f32_16x16x128_f8f6f4 v[72:75], v[8:15], v[56:63], v[72:75], v235, v235 op_sel_hi:[0,0,0]
	v_mfma_scale_f32_16x16x128_f8f6f4 v[68:71], v[0:7], v[56:63], v[68:71], v235, v235 op_sel_hi:[0,0,0]
	s_setprio 0
	s_barrier
	s_andn2_b64 vcc, exec, s[20:21]
	s_cbranch_vccnz .LBB0_1371
	s_barrier

.LBB0_1452:
	s_add_i32 s33, s80, 0x180
	s_add_i32 s36, s81, 0x180
	s_waitcnt lgkmcnt(0)
	s_barrier
	s_setprio 1
	v_mfma_scale_f32_16x16x128_f8f6f4 v[128:131], v[24:31], v[56:63], 0, v235, v235 op_sel_hi:[0,0,0]
	v_mfma_scale_f32_16x16x128_f8f6f4 v[124:127], v[16:23], v[56:63], 0, v235, v235 op_sel_hi:[0,0,0]
	v_mfma_scale_f32_16x16x128_f8f6f4 v[120:123], v[24:31], v[48:55], 0, v235, v235 op_sel_hi:[0,0,0]
	v_mfma_scale_f32_16x16x128_f8f6f4 v[116:119], v[16:23], v[48:55], 0, v235, v235 op_sel_hi:[0,0,0]
	v_mfma_scale_f32_16x16x128_f8f6f4 v[112:115], v[24:31], v[40:47], 0, v235, v235 op_sel_hi:[0,0,0]
	v_mfma_scale_f32_16x16x128_f8f6f4 v[108:111], v[16:23], v[40:47], 0, v235, v235 op_sel_hi:[0,0,0]
	v_mfma_scale_f32_16x16x128_f8f6f4 v[104:107], v[24:31], v[32:39], 0, v235, v235 op_sel_hi:[0,0,0]
	v_mfma_scale_f32_16x16x128_f8f6f4 v[100:103], v[16:23], v[32:39], 0, v235, v235 op_sel_hi:[0,0,0]
	s_setprio 0
	s_setprio 1
	v_mfma_scale_f32_16x16x128_f8f6f4 v[96:99], v[8:15], v[56:63], 0, v235, v235 op_sel_hi:[0,0,0]
	v_mfma_scale_f32_16x16x128_f8f6f4 v[92:95], v[0:7], v[56:63], 0, v235, v235 op_sel_hi:[0,0,0]
	v_mfma_scale_f32_16x16x128_f8f6f4 v[88:91], v[8:15], v[48:55], 0, v235, v235 op_sel_hi:[0,0,0]
	v_mfma_scale_f32_16x16x128_f8f6f4 v[84:87], v[0:7], v[48:55], 0, v235, v235 op_sel_hi:[0,0,0]
	v_mfma_scale_f32_16x16x128_f8f6f4 v[80:83], v[8:15], v[40:47], 0, v235, v235 op_sel_hi:[0,0,0]
	v_mfma_scale_f32_16x16x128_f8f6f4 v[76:79], v[0:7], v[40:47], 0, v235, v235 op_sel_hi:[0,0,0]
	v_mfma_scale_f32_16x16x128_f8f6f4 v[72:75], v[8:15], v[32:39], 0, v235, v235 op_sel_hi:[0,0,0]
	v_mfma_scale_f32_16x16x128_f8f6f4 v[68:71], v[0:7], v[32:39], 0, v235, v235 op_sel_hi:[0,0,0]
	s_setprio 0
	s_barrier
	ds_read_b128 v[16:19], v233 offset:0x8000
	ds_read_b128 v[20:23], v233 offset:0x8400
	ds_read_b128 v[24:27], v233 offset:0x8800
	ds_read_b128 v[28:31], v233 offset:0x8c00
	ds_read_b128 v[32:35], v232 offset:0x8000
	ds_read_b128 v[36:39], v232 offset:0x8400
	ds_read_b128 v[40:43], v232 offset:0x8800
	ds_read_b128 v[44:47], v232 offset:0x8c00
	ds_read_b128 v[48:51], v232 offset:0x9000
	ds_read_b128 v[52:55], v232 offset:0x9400
	ds_read_b128 v[56:59], v232 offset:0x9800
	ds_read_b128 v[60:63], v232 offset:0x9c00
	ds_read_b128 v[8:11], v233 offset:0xc000
	ds_read_b128 v[12:15], v233 offset:0xc400
	ds_read_b128 v[0:3], v233 offset:0xc800
	ds_read_b128 v[4:7], v233 offset:0xcc00
	s_mov_b32 m0, s62
	s_add_i32 s10, s80, 0x10100
	buffer_load_dwordx4 v230, s[4:7], s10 offen lds
	s_add_i32 s10, s80, 0x18100
	s_mov_b32 m0, s63
	s_nop 0
	buffer_load_dwordx4 v230, s[4:7], s10 offen lds
	s_waitcnt vmcnt(8)
	s_waitcnt lgkmcnt(0)
	s_barrier
	s_setprio 1
	v_mfma_scale_f32_16x16x128_f8f6f4 v[192:195], v[16:23], v[32:39], v[192:195], v235, v235 op_sel_hi:[0,0,0]
	v_mfma_scale_f32_16x16x128_f8f6f4 v[188:191], v[24:31], v[32:39], v[188:191], v235, v235 op_sel_hi:[0,0,0]
	v_mfma_scale_f32_16x16x128_f8f6f4 v[184:187], v[16:23], v[40:47], v[184:187], v235, v235 op_sel_hi:[0,0,0]
	v_mfma_scale_f32_16x16x128_f8f6f4 v[180:183], v[24:31], v[40:47], v[180:183], v235, v235 op_sel_hi:[0,0,0]
	v_mfma_scale_f32_16x16x128_f8f6f4 v[176:179], v[16:23], v[48:55], v[176:179], v235, v235 op_sel_hi:[0,0,0]
	v_mfma_scale_f32_16x16x128_f8f6f4 v[172:175], v[24:31], v[48:55], v[172:175], v235, v235 op_sel_hi:[0,0,0]
	v_mfma_scale_f32_16x16x128_f8f6f4 v[168:171], v[16:23], v[56:63], v[168:171], v235, v235 op_sel_hi:[0,0,0]
	v_mfma_scale_f32_16x16x128_f8f6f4 v[164:167], v[24:31], v[56:63], v[164:167], v235, v235 op_sel_hi:[0,0,0]
	s_setprio 0
	s_setprio 1
	v_mfma_scale_f32_16x16x128_f8f6f4 v[160:163], v[8:15], v[32:39], v[160:163], v235, v235 op_sel_hi:[0,0,0]
	v_mfma_scale_f32_16x16x128_f8f6f4 v[156:159], v[0:7], v[32:39], v[156:159], v235, v235 op_sel_hi:[0,0,0]
	v_mfma_scale_f32_16x16x128_f8f6f4 v[152:155], v[8:15], v[40:47], v[152:155], v235, v235 op_sel_hi:[0,0,0]
	v_mfma_scale_f32_16x16x128_f8f6f4 v[148:151], v[0:7], v[40:47], v[148:151], v235, v235 op_sel_hi:[0,0,0]
	v_mfma_scale_f32_16x16x128_f8f6f4 v[144:147], v[8:15], v[48:55], v[144:147], v235, v235 op_sel_hi:[0,0,0]
	v_mfma_scale_f32_16x16x128_f8f6f4 v[140:143], v[0:7], v[48:55], v[140:143], v235, v235 op_sel_hi:[0,0,0]
	v_mfma_scale_f32_16x16x128_f8f6f4 v[136:139], v[8:15], v[56:63], v[136:139], v235, v235 op_sel_hi:[0,0,0]
	v_mfma_scale_f32_16x16x128_f8f6f4 v[132:135], v[0:7], v[56:63], v[132:135], v235, v235 op_sel_hi:[0,0,0]
	s_setprio 0
	s_barrier
	ds_read_b128 v[32:35], v232 offset:0xc000
	ds_read_b128 v[36:39], v232 offset:0xc400
	ds_read_b128 v[40:43], v232 offset:0xc800
	ds_read_b128 v[44:47], v232 offset:0xcc00
	ds_read_b128 v[48:51], v232 offset:0xd000
	ds_read_b128 v[52:55], v232 offset:0xd400
	ds_read_b128 v[56:59], v232 offset:0xd800
	ds_read_b128 v[60:63], v232 offset:0xdc00
	s_mov_b32 m0, s64
	s_mov_b32 s10, s6
	s_mov_b32 s11, s7
	buffer_load_dwordx4 v231, s[8:11], s36 offen lds
	s_add_i32 s36, s81, 0x10180
	s_mov_b32 m0, s65
	s_nop 0
	buffer_load_dwordx4 v231, s[8:11], s36 offen lds
	s_add_i32 s36, s81, 0x1180
	s_mov_b32 m0, s70
	s_nop 0
	buffer_load_dwordx4 v231, s[8:11], s36 offen lds
	s_add_i32 s36, s81, 0x11180
	s_mov_b32 m0, s71
	s_nop 0
	buffer_load_dwordx4 v231, s[8:11], s36 offen lds
	s_mov_b32 m0, s68
	s_nop 0
	buffer_load_dwordx4 v230, s[4:7], s33 offen lds
	s_add_i32 s33, s80, 0x8180
	s_mov_b32 m0, s69
	s_nop 0
	buffer_load_dwordx4 v230, s[4:7], s33 offen lds
	s_waitcnt vmcnt(8)
	s_waitcnt lgkmcnt(0)
	s_barrier
	s_setprio 1
	v_mfma_scale_f32_16x16x128_f8f6f4 v[128:131], v[16:23], v[32:39], v[128:131], v235, v235 op_sel_hi:[0,0,0]
	v_mfma_scale_f32_16x16x128_f8f6f4 v[124:127], v[24:31], v[32:39], v[124:127], v235, v235 op_sel_hi:[0,0,0]
	v_mfma_scale_f32_16x16x128_f8f6f4 v[120:123], v[16:23], v[40:47], v[120:123], v235, v235 op_sel_hi:[0,0,0]
	v_mfma_scale_f32_16x16x128_f8f6f4 v[116:119], v[24:31], v[40:47], v[116:119], v235, v235 op_sel_hi:[0,0,0]
	v_mfma_scale_f32_16x16x128_f8f6f4 v[112:115], v[16:23], v[48:55], v[112:115], v235, v235 op_sel_hi:[0,0,0]
	v_mfma_scale_f32_16x16x128_f8f6f4 v[108:111], v[24:31], v[48:55], v[108:111], v235, v235 op_sel_hi:[0,0,0]
	v_mfma_scale_f32_16x16x128_f8f6f4 v[104:107], v[16:23], v[56:63], v[104:107], v235, v235 op_sel_hi:[0,0,0]
	v_mfma_scale_f32_16x16x128_f8f6f4 v[100:103], v[24:31], v[56:63], v[100:103], v235, v235 op_sel_hi:[0,0,0]
	s_setprio 0
	s_setprio 1
	v_mfma_scale_f32_16x16x128_f8f6f4 v[96:99], v[8:15], v[32:39], v[96:99], v235, v235 op_sel_hi:[0,0,0]
	v_mfma_scale_f32_16x16x128_f8f6f4 v[92:95], v[0:7], v[32:39], v[92:95], v235, v235 op_sel_hi:[0,0,0]
	v_mfma_scale_f32_16x16x128_f8f6f4 v[88:91], v[8:15], v[40:47], v[88:91], v235, v235 op_sel_hi:[0,0,0]
	v_mfma_scale_f32_16x16x128_f8f6f4 v[84:87], v[0:7], v[40:47], v[84:87], v235, v235 op_sel_hi:[0,0,0]
	v_mfma_scale_f32_16x16x128_f8f6f4 v[80:83], v[8:15], v[48:55], v[80:83], v235, v235 op_sel_hi:[0,0,0]
	v_mfma_scale_f32_16x16x128_f8f6f4 v[76:79], v[0:7], v[48:55], v[76:79], v235, v235 op_sel_hi:[0,0,0]
	v_mfma_scale_f32_16x16x128_f8f6f4 v[72:75], v[8:15], v[56:63], v[72:75], v235, v235 op_sel_hi:[0,0,0]
	v_mfma_scale_f32_16x16x128_f8f6f4 v[68:71], v[0:7], v[56:63], v[68:71], v235, v235 op_sel_hi:[0,0,0]
	s_setprio 0
	s_barrier
	ds_read_b128 v[16:19], v233 offset:0
	ds_read_b128 v[20:23], v233 offset:0x400
	ds_read_b128 v[24:27], v233 offset:0x800
	ds_read_b128 v[28:31], v233 offset:0xc00
	ds_read_b128 v[32:35], v232 offset:0
	ds_read_b128 v[36:39], v232 offset:0x400
	ds_read_b128 v[40:43], v232 offset:0x800
	ds_read_b128 v[44:47], v232 offset:0xc00
	ds_read_b128 v[48:51], v232 offset:0x1000
	ds_read_b128 v[52:55], v232 offset:0x1400
	ds_read_b128 v[56:59], v232 offset:0x1800
	ds_read_b128 v[60:63], v232 offset:0x1c00
	ds_read_b128 v[8:11], v233 offset:0x4000
	ds_read_b128 v[12:15], v233 offset:0x4400
	ds_read_b128 v[0:3], v233 offset:0x4800
	ds_read_b128 v[4:7], v233 offset:0x4c00
	s_add_i32 s33, s43, 0x80
	s_mov_b32 m0, s74
	s_add_i32 s36, s80, 0x10180
	buffer_load_dwordx4 v230, s[4:7], s36 offen lds
	s_add_i32 s36, s80, 0x18180
	s_mov_b32 m0, s76
	s_nop 0
	buffer_load_dwordx4 v230, s[4:7], s36 offen lds
	s_waitcnt vmcnt(8)
	s_waitcnt lgkmcnt(0)
	s_barrier
	s_setprio 1
	v_mfma_scale_f32_16x16x128_f8f6f4 v[192:195], v[16:23], v[32:39], v[192:195], v235, v235 op_sel_hi:[0,0,0]
	v_mfma_scale_f32_16x16x128_f8f6f4 v[188:191], v[24:31], v[32:39], v[188:191], v235, v235 op_sel_hi:[0,0,0]
	v_mfma_scale_f32_16x16x128_f8f6f4 v[184:187], v[16:23], v[40:47], v[184:187], v235, v235 op_sel_hi:[0,0,0]
	v_mfma_scale_f32_16x16x128_f8f6f4 v[180:183], v[24:31], v[40:47], v[180:183], v235, v235 op_sel_hi:[0,0,0]
	v_mfma_scale_f32_16x16x128_f8f6f4 v[176:179], v[16:23], v[48:55], v[176:179], v235, v235 op_sel_hi:[0,0,0]
	v_mfma_scale_f32_16x16x128_f8f6f4 v[172:175], v[24:31], v[48:55], v[172:175], v235, v235 op_sel_hi:[0,0,0]
	v_mfma_scale_f32_16x16x128_f8f6f4 v[168:171], v[16:23], v[56:63], v[168:171], v235, v235 op_sel_hi:[0,0,0]
	v_mfma_scale_f32_16x16x128_f8f6f4 v[164:167], v[24:31], v[56:63], v[164:167], v235, v235 op_sel_hi:[0,0,0]
	s_setprio 0
	s_setprio 1
	v_mfma_scale_f32_16x16x128_f8f6f4 v[160:163], v[8:15], v[32:39], v[160:163], v235, v235 op_sel_hi:[0,0,0]
	v_mfma_scale_f32_16x16x128_f8f6f4 v[156:159], v[0:7], v[32:39], v[156:159], v235, v235 op_sel_hi:[0,0,0]
	v_mfma_scale_f32_16x16x128_f8f6f4 v[152:155], v[8:15], v[40:47], v[152:155], v235, v235 op_sel_hi:[0,0,0]
	v_mfma_scale_f32_16x16x128_f8f6f4 v[148:151], v[0:7], v[40:47], v[148:151], v235, v235 op_sel_hi:[0,0,0]
	v_mfma_scale_f32_16x16x128_f8f6f4 v[144:147], v[8:15], v[48:55], v[144:147], v235, v235 op_sel_hi:[0,0,0]
	v_mfma_scale_f32_16x16x128_f8f6f4 v[140:143], v[0:7], v[48:55], v[140:143], v235, v235 op_sel_hi:[0,0,0]
	v_mfma_scale_f32_16x16x128_f8f6f4 v[136:139], v[8:15], v[56:63], v[136:139], v235, v235 op_sel_hi:[0,0,0]
	v_mfma_scale_f32_16x16x128_f8f6f4 v[132:135], v[0:7], v[56:63], v[132:135], v235, v235 op_sel_hi:[0,0,0]
	s_setprio 0
	s_barrier
	ds_read_b128 v[32:35], v232 offset:0x4000
	ds_read_b128 v[36:39], v232 offset:0x4400
	ds_read_b128 v[40:43], v232 offset:0x4800
	ds_read_b128 v[44:47], v232 offset:0x4c00
	ds_read_b128 v[48:51], v232 offset:0x5000
	ds_read_b128 v[52:55], v232 offset:0x5400
	ds_read_b128 v[56:59], v232 offset:0x5800
	ds_read_b128 v[60:63], v232 offset:0x5c00
	s_mov_b32 m0, s46
	s_nop 0
	buffer_load_dwordx4 v231, s[8:11], s78 offen lds
	s_add_i32 s36, s78, 0x10000
	s_mov_b32 m0, s47
	s_nop 0
	buffer_load_dwordx4 v231, s[8:11], s36 offen lds
	s_add_i32 s36, s78, 0x1000
	s_mov_b32 m0, s49
	s_nop 0
	buffer_load_dwordx4 v231, s[8:11], s36 offen lds
	s_add_i32 s36, s78, 0x11000
	s_mov_b32 m0, s50
	s_nop 0
	buffer_load_dwordx4 v231, s[8:11], s36 offen lds
	s_mov_b32 m0, s48
	s_add_i32 s36, s43, 0x8000
	buffer_load_dwordx4 v230, s[4:7], s43 offen lds
	s_mov_b32 m0, s51
	s_nop 0
	buffer_load_dwordx4 v230, s[4:7], s36 offen lds
	s_waitcnt vmcnt(8)
	s_waitcnt lgkmcnt(0)
	s_barrier
	s_setprio 1
	v_mfma_scale_f32_16x16x128_f8f6f4 v[128:131], v[16:23], v[32:39], v[128:131], v235, v235 op_sel_hi:[0,0,0]
	v_mfma_scale_f32_16x16x128_f8f6f4 v[124:127], v[24:31], v[32:39], v[124:127], v235, v235 op_sel_hi:[0,0,0]
	v_mfma_scale_f32_16x16x128_f8f6f4 v[120:123], v[16:23], v[40:47], v[120:123], v235, v235 op_sel_hi:[0,0,0]
	v_mfma_scale_f32_16x16x128_f8f6f4 v[116:119], v[24:31], v[40:47], v[116:119], v235, v235 op_sel_hi:[0,0,0]
	v_mfma_scale_f32_16x16x128_f8f6f4 v[112:115], v[16:23], v[48:55], v[112:115], v235, v235 op_sel_hi:[0,0,0]
	v_mfma_scale_f32_16x16x128_f8f6f4 v[108:111], v[24:31], v[48:55], v[108:111], v235, v235 op_sel_hi:[0,0,0]
	v_mfma_scale_f32_16x16x128_f8f6f4 v[104:107], v[16:23], v[56:63], v[104:107], v235, v235 op_sel_hi:[0,0,0]
	v_mfma_scale_f32_16x16x128_f8f6f4 v[100:103], v[24:31], v[56:63], v[100:103], v235, v235 op_sel_hi:[0,0,0]
	s_setprio 0
	s_setprio 1
	v_mfma_scale_f32_16x16x128_f8f6f4 v[96:99], v[8:15], v[32:39], v[96:99], v235, v235 op_sel_hi:[0,0,0]
	v_mfma_scale_f32_16x16x128_f8f6f4 v[92:95], v[0:7], v[32:39], v[92:95], v235, v235 op_sel_hi:[0,0,0]
	v_mfma_scale_f32_16x16x128_f8f6f4 v[88:91], v[8:15], v[40:47], v[88:91], v235, v235 op_sel_hi:[0,0,0]
	v_mfma_scale_f32_16x16x128_f8f6f4 v[84:87], v[0:7], v[40:47], v[84:87], v235, v235 op_sel_hi:[0,0,0]
	v_mfma_scale_f32_16x16x128_f8f6f4 v[80:83], v[8:15], v[48:55], v[80:83], v235, v235 op_sel_hi:[0,0,0]
	v_mfma_scale_f32_16x16x128_f8f6f4 v[76:79], v[0:7], v[48:55], v[76:79], v235, v235 op_sel_hi:[0,0,0]
	v_mfma_scale_f32_16x16x128_f8f6f4 v[72:75], v[8:15], v[56:63], v[72:75], v235, v235 op_sel_hi:[0,0,0]
	v_mfma_scale_f32_16x16x128_f8f6f4 v[68:71], v[0:7], v[56:63], v[68:71], v235, v235 op_sel_hi:[0,0,0]
	s_setprio 0
	s_barrier
	ds_read_b128 v[16:19], v233 offset:0x8000
	ds_read_b128 v[20:23], v233 offset:0x8400
	ds_read_b128 v[24:27], v233 offset:0x8800
	ds_read_b128 v[28:31], v233 offset:0x8c00
	ds_read_b128 v[32:35], v232 offset:0x8000
	ds_read_b128 v[36:39], v232 offset:0x8400
	ds_read_b128 v[40:43], v232 offset:0x8800
	ds_read_b128 v[44:47], v232 offset:0x8c00
	ds_read_b128 v[48:51], v232 offset:0x9000
	ds_read_b128 v[52:55], v232 offset:0x9400
	ds_read_b128 v[56:59], v232 offset:0x9800
	ds_read_b128 v[60:63], v232 offset:0x9c00
	ds_read_b128 v[8:11], v233 offset:0xc000
	ds_read_b128 v[12:15], v233 offset:0xc400
	ds_read_b128 v[0:3], v233 offset:0xc800
	ds_read_b128 v[4:7], v233 offset:0xcc00
	s_mov_b32 m0, s62
	s_add_i32 s36, s43, 0x10000
	buffer_load_dwordx4 v230, s[4:7], s36 offen lds
	s_add_i32 s36, s43, 0x18000
	s_mov_b32 m0, s63
	s_nop 0
	buffer_load_dwordx4 v230, s[4:7], s36 offen lds
	s_waitcnt vmcnt(8)
	s_waitcnt lgkmcnt(0)
	s_barrier
	s_setprio 1
	v_mfma_scale_f32_16x16x128_f8f6f4 v[192:195], v[16:23], v[32:39], v[192:195], v235, v235 op_sel_hi:[0,0,0]
	v_mfma_scale_f32_16x16x128_f8f6f4 v[188:191], v[24:31], v[32:39], v[188:191], v235, v235 op_sel_hi:[0,0,0]
	v_mfma_scale_f32_16x16x128_f8f6f4 v[184:187], v[16:23], v[40:47], v[184:187], v235, v235 op_sel_hi:[0,0,0]
	v_mfma_scale_f32_16x16x128_f8f6f4 v[180:183], v[24:31], v[40:47], v[180:183], v235, v235 op_sel_hi:[0,0,0]
	v_mfma_scale_f32_16x16x128_f8f6f4 v[176:179], v[16:23], v[48:55], v[176:179], v235, v235 op_sel_hi:[0,0,0]
	v_mfma_scale_f32_16x16x128_f8f6f4 v[172:175], v[24:31], v[48:55], v[172:175], v235, v235 op_sel_hi:[0,0,0]
	v_mfma_scale_f32_16x16x128_f8f6f4 v[168:171], v[16:23], v[56:63], v[168:171], v235, v235 op_sel_hi:[0,0,0]
	v_mfma_scale_f32_16x16x128_f8f6f4 v[164:167], v[24:31], v[56:63], v[164:167], v235, v235 op_sel_hi:[0,0,0]
	s_setprio 0
	s_setprio 1
	v_mfma_scale_f32_16x16x128_f8f6f4 v[160:163], v[8:15], v[32:39], v[160:163], v235, v235 op_sel_hi:[0,0,0]
	v_mfma_scale_f32_16x16x128_f8f6f4 v[156:159], v[0:7], v[32:39], v[156:159], v235, v235 op_sel_hi:[0,0,0]
	v_mfma_scale_f32_16x16x128_f8f6f4 v[152:155], v[8:15], v[40:47], v[152:155], v235, v235 op_sel_hi:[0,0,0]
	v_mfma_scale_f32_16x16x128_f8f6f4 v[148:151], v[0:7], v[40:47], v[148:151], v235, v235 op_sel_hi:[0,0,0]
	v_mfma_scale_f32_16x16x128_f8f6f4 v[144:147], v[8:15], v[48:55], v[144:147], v235, v235 op_sel_hi:[0,0,0]
	v_mfma_scale_f32_16x16x128_f8f6f4 v[140:143], v[0:7], v[48:55], v[140:143], v235, v235 op_sel_hi:[0,0,0]
	v_mfma_scale_f32_16x16x128_f8f6f4 v[136:139], v[8:15], v[56:63], v[136:139], v235, v235 op_sel_hi:[0,0,0]
	v_mfma_scale_f32_16x16x128_f8f6f4 v[132:135], v[0:7], v[56:63], v[132:135], v235, v235 op_sel_hi:[0,0,0]
	s_setprio 0
	s_barrier
	ds_read_b128 v[32:35], v232 offset:0xc000
	ds_read_b128 v[36:39], v232 offset:0xc400
	ds_read_b128 v[40:43], v232 offset:0xc800
	ds_read_b128 v[44:47], v232 offset:0xcc00
	ds_read_b128 v[48:51], v232 offset:0xd000
	ds_read_b128 v[52:55], v232 offset:0xd400
	ds_read_b128 v[56:59], v232 offset:0xd800
	ds_read_b128 v[60:63], v232 offset:0xdc00
	s_mov_b32 m0, s64
	s_add_i32 s36, s78, 0x80
	buffer_load_dwordx4 v231, s[8:11], s36 offen lds
	s_add_i32 s36, s78, 0x10080
	s_mov_b32 m0, s65
	s_nop 0
	buffer_load_dwordx4 v231, s[8:11], s36 offen lds
	s_add_i32 s36, s78, 0x1080
	s_mov_b32 m0, s70
	s_nop 0
	buffer_load_dwordx4 v231, s[8:11], s36 offen lds
	s_add_i32 s36, s78, 0x11080
	s_mov_b32 m0, s71
	s_nop 0
	buffer_load_dwordx4 v231, s[8:11], s36 offen lds
	s_mov_b32 m0, s68
	s_add_i32 s10, s43, 0x8080
	buffer_load_dwordx4 v230, s[4:7], s33 offen lds
	s_mov_b32 m0, s69
	s_nop 0
	buffer_load_dwordx4 v230, s[4:7], s10 offen lds
	s_waitcnt vmcnt(8)
	s_waitcnt lgkmcnt(0)
	s_barrier
	s_setprio 1
	v_mfma_scale_f32_16x16x128_f8f6f4 v[128:131], v[16:23], v[32:39], v[128:131], v235, v235 op_sel_hi:[0,0,0]
	v_mfma_scale_f32_16x16x128_f8f6f4 v[124:127], v[24:31], v[32:39], v[124:127], v235, v235 op_sel_hi:[0,0,0]
	v_mfma_scale_f32_16x16x128_f8f6f4 v[120:123], v[16:23], v[40:47], v[120:123], v235, v235 op_sel_hi:[0,0,0]
	v_mfma_scale_f32_16x16x128_f8f6f4 v[116:119], v[24:31], v[40:47], v[116:119], v235, v235 op_sel_hi:[0,0,0]
	v_mfma_scale_f32_16x16x128_f8f6f4 v[112:115], v[16:23], v[48:55], v[112:115], v235, v235 op_sel_hi:[0,0,0]
	v_mfma_scale_f32_16x16x128_f8f6f4 v[108:111], v[24:31], v[48:55], v[108:111], v235, v235 op_sel_hi:[0,0,0]
	v_mfma_scale_f32_16x16x128_f8f6f4 v[104:107], v[16:23], v[56:63], v[104:107], v235, v235 op_sel_hi:[0,0,0]
	v_mfma_scale_f32_16x16x128_f8f6f4 v[100:103], v[24:31], v[56:63], v[100:103], v235, v235 op_sel_hi:[0,0,0]
	s_setprio 0
	s_setprio 1
	v_mfma_scale_f32_16x16x128_f8f6f4 v[96:99], v[8:15], v[32:39], v[96:99], v235, v235 op_sel_hi:[0,0,0]
	v_mfma_scale_f32_16x16x128_f8f6f4 v[92:95], v[0:7], v[32:39], v[92:95], v235, v235 op_sel_hi:[0,0,0]
	v_mfma_scale_f32_16x16x128_f8f6f4 v[88:91], v[8:15], v[40:47], v[88:91], v235, v235 op_sel_hi:[0,0,0]
	v_mfma_scale_f32_16x16x128_f8f6f4 v[84:87], v[0:7], v[40:47], v[84:87], v235, v235 op_sel_hi:[0,0,0]
	v_mfma_scale_f32_16x16x128_f8f6f4 v[80:83], v[8:15], v[48:55], v[80:83], v235, v235 op_sel_hi:[0,0,0]
	v_mfma_scale_f32_16x16x128_f8f6f4 v[76:79], v[0:7], v[48:55], v[76:79], v235, v235 op_sel_hi:[0,0,0]
	v_mfma_scale_f32_16x16x128_f8f6f4 v[72:75], v[8:15], v[56:63], v[72:75], v235, v235 op_sel_hi:[0,0,0]
	v_mfma_scale_f32_16x16x128_f8f6f4 v[68:71], v[0:7], v[56:63], v[68:71], v235, v235 op_sel_hi:[0,0,0]
	s_setprio 0
	s_barrier
	s_andn2_b64 vcc, exec, s[20:21]
	s_cbranch_vccnz .LBB0_1454
	s_barrier
